# GEMM epilogues P5/P6/P9/P10: serialized load->vmcnt(0)->store chains replaced by hoisted loads into dead fragment VGPRs with counted waits
# speedup vs baseline: 1.0030x; 1.0030x over previous
; DI unsigned cvt_pk_bf16(float lo, float hi) { unsigned r; asm volatile("v_cvt_pk_bf16_f32 %0, %1, %2" : "=v"(r) : "v"(lo), "v"(hi)); return r; }
;     DI void operator()(const f32x4 (&acc)[2][2][4][2], const pg8::Unit& u, int wr, int wc, int fr, int fq) const {
;         const int row0 = u.pm * 256 + wr * 64 + fr, col0 = u.pn * 256 + wc * 32 + 8 * fq;
; #pragma unroll
;         for (int ai = 0; ai < 2; ++ai)
; #pragma unroll
;             for (int m = 0; m < 4; ++m)
; #pragma unroll
;                 for (int bj = 0; bj < 2; ++bj) {
;                     const size_t o = (size_t)(row0 + ai * 128 + m * 16) * D + col0 + bj * 128;
;                     const u32x4 gt = *(const u32x4*)(ga + o);
;                     float v[8];
; #pragma unroll
;                     for (int e = 0; e < 4; ++e) { v[e] = acc[ai][bj][m][0][e]; v[4 + e] = acc[ai][bj][m][1][e]; }
;                     v[0] *= bflo(gt.x); v[1] *= bfhi(gt.x); v[2] *= bflo(gt.y); v[3] *= bfhi(gt.y); v[4] *= bflo(gt.z); v[5] *= bfhi(gt.z); v[6] *= bflo(gt.w); v[7] *= bfhi(gt.w);
;                     u32x4 w; w.x = pg8::cvt_pk_bf16(v[0], v[1]); w.y = pg8::cvt_pk_bf16(v[2], v[3]); w.z = pg8::cvt_pk_bf16(v[4], v[5]); w.w = pg8::cvt_pk_bf16(v[6], v[7]);
;                     *(u32x4*)(outp + o) = w;
;                 }
;     }
.LBB0_606:
	v_add_u32_e32 v150, s78, v179
	v_or_b32_e32 v152, s79, v181
	v_ashrrev_i32_e32 v151, 31, v150
	v_ashrrev_i32_e32 v153, 31, v152
	v_lshlrev_b64 v[154:155], 11, v[150:151]
	v_lshl_add_u64 v[172:173], v[154:155], 0, v[152:153]
	v_lshlrev_b64 v[154:155], 1, v[172:173]
	v_lshl_add_u64 v[172:173], s[12:13], 0, v[154:155]
	global_load_dwordx4 v[184:187], v[172:173], off
	v_or_b32_e32 v172, 0x100, v154
	v_mov_b32_e32 v173, v155
	v_lshl_add_u64 v[174:175], s[12:13], 0, v[172:173]
	global_load_dwordx4 v[188:191], v[174:175], off
	v_or_b32_e32 v172, 16, v150
	v_ashrrev_i32_e32 v173, 31, v172
	v_lshlrev_b64 v[174:175], 11, v[172:173]
	v_lshl_add_u64 v[172:173], v[174:175], 0, v[152:153]
	v_lshlrev_b64 v[174:175], 1, v[172:173]
	v_lshl_add_u64 v[172:173], s[12:13], 0, v[174:175]
	global_load_dwordx4 v[192:195], v[172:173], off
	v_or_b32_e32 v174, 0x100, v174
	v_lshl_add_u64 v[172:173], s[12:13], 0, v[174:175]
	global_load_dwordx4 v[196:199], v[172:173], off
	v_or_b32_e32 v172, 32, v150
	v_ashrrev_i32_e32 v173, 31, v172
	v_lshlrev_b64 v[174:175], 11, v[172:173]
	v_lshl_add_u64 v[172:173], v[174:175], 0, v[152:153]
	v_lshlrev_b64 v[174:175], 1, v[172:173]
	v_lshl_add_u64 v[172:173], s[12:13], 0, v[174:175]
	global_load_dwordx4 v[200:203], v[172:173], off
	v_or_b32_e32 v174, 0x100, v174
	v_lshl_add_u64 v[172:173], s[12:13], 0, v[174:175]
	global_load_dwordx4 v[204:207], v[172:173], off
	v_or_b32_e32 v172, 48, v150
	v_ashrrev_i32_e32 v173, 31, v172
	v_lshlrev_b64 v[150:151], 11, v[172:173]
	v_lshl_add_u64 v[172:173], v[150:151], 0, v[152:153]
	v_lshlrev_b64 v[150:151], 1, v[172:173]
	v_lshl_add_u64 v[152:153], s[12:13], 0, v[150:151]
	global_load_dwordx4 v[208:211], v[152:153], off
	v_or_b32_e32 v150, 0x100, v150
	v_lshl_add_u64 v[152:153], s[12:13], 0, v[150:151]
	global_load_dwordx4 v[212:215], v[152:153], off
	v_lshl_add_u64 v[150:151], v[154:155], 0, s[28:29]
	v_lshl_add_u64 v[152:153], s[12:13], 0, v[150:151]
	global_load_dwordx4 v[216:219], v[152:153], off
	v_lshl_add_u64 v[150:151], v[154:155], 0, s[36:37]
	v_lshl_add_u64 v[152:153], s[12:13], 0, v[150:151]
	global_load_dwordx4 v[220:223], v[152:153], off
	v_lshl_add_u64 v[150:151], v[154:155], 0, s[30:31]
	v_lshl_add_u64 v[152:153], s[12:13], 0, v[150:151]
	global_load_dwordx4 v[224:227], v[152:153], off
	v_lshl_add_u64 v[150:151], v[154:155], 0, s[40:41]
	v_lshl_add_u64 v[152:153], s[12:13], 0, v[150:151]
	global_load_dwordx4 v[228:231], v[152:153], off
	v_lshl_add_u64 v[150:151], v[154:155], 0, s[8:9]
	v_lshl_add_u64 v[152:153], s[12:13], 0, v[150:151]
	global_load_dwordx4 v[232:235], v[152:153], off
	v_lshl_add_u64 v[150:151], v[154:155], 0, s[42:43]
	v_lshl_add_u64 v[152:153], s[12:13], 0, v[150:151]
	global_load_dwordx4 v[236:239], v[152:153], off
	v_lshl_add_u64 v[150:151], v[154:155], 0, s[34:35]
	v_lshl_add_u64 v[152:153], s[12:13], 0, v[150:151]
	global_load_dwordx4 v[240:243], v[152:153], off
	v_lshl_add_u64 v[150:151], v[154:155], 0, s[44:45]
	v_lshl_add_u64 v[152:153], s[12:13], 0, v[150:151]
	global_load_dwordx4 v[244:247], v[152:153], off
	v_add_u32_e32 v136, s78, v179
	v_or_b32_e32 v134, s79, v181
	v_ashrrev_i32_e32 v137, 31, v136
	v_ashrrev_i32_e32 v135, 31, v134
	v_lshlrev_b64 v[132:133], 11, v[136:137]
	v_lshl_add_u64 v[132:133], v[132:133], 0, v[134:135]
	v_lshlrev_b64 v[132:133], 1, v[132:133]
	v_lshl_add_u64 v[138:139], s[12:13], 0, v[132:133]
	s_nop 0
	v_lshl_add_u64 v[142:143], s[16:17], 0, v[132:133]
	v_or_b32_e32 v144, 0x100, v132
	v_mov_b32_e32 v145, v133
	v_lshl_add_u64 v[146:147], s[12:13], 0, v[144:145]
	s_and_b64 vcc, exec, s[6:7]
	s_mov_b64 s[6:7], -1
	s_nop 0
	s_waitcnt vmcnt(15)
	v_lshlrev_b32_e32 v149, 16, v187
	v_and_b32_e32 v141, 0xffff0000, v187
	v_lshlrev_b32_e32 v3, 16, v184
	v_and_b32_e32 v137, 0xffff0000, v184
	v_lshlrev_b32_e32 v138, 16, v185
	v_and_b32_e32 v139, 0xffff0000, v185
	v_lshlrev_b32_e32 v148, 16, v186
	v_and_b32_e32 v140, 0xffff0000, v186
	v_mul_f32_e32 v127, v127, v141
	v_mul_f32_e32 v3, v128, v3
	v_mul_f32_e32 v128, v129, v137
	v_mul_f32_e32 v129, v130, v138
	v_mul_f32_e32 v130, v131, v139
	v_mul_f32_e32 v131, v124, v148
	v_mul_f32_e32 v137, v125, v140
	v_mul_f32_e32 v138, v126, v149
	v_cvt_pk_bf16_f32 v124, v3, v128
	v_cvt_pk_bf16_f32 v125, v129, v130
	v_cvt_pk_bf16_f32 v126, v131, v137
	v_cvt_pk_bf16_f32 v127, v138, v127
	global_store_dwordx4 v[142:143], v[124:127], off
	s_nop 0
	v_or_b32_e32 v128, 16, v136
	v_ashrrev_i32_e32 v129, 31, v128
	v_lshlrev_b64 v[128:129], 11, v[128:129]
	v_lshl_add_u64 v[128:129], v[128:129], 0, v[134:135]
	v_lshlrev_b64 v[128:129], 1, v[128:129]
	v_lshl_add_u64 v[130:131], s[16:17], 0, v[144:145]
	v_lshl_add_u64 v[138:139], s[12:13], 0, v[128:129]
	s_nop 0
	s_waitcnt vmcnt(15)
	v_lshlrev_b32_e32 v141, 16, v191
	v_and_b32_e32 v127, 0xffff0000, v191
	v_lshlrev_b32_e32 v3, 16, v188
	v_and_b32_e32 v124, 0xffff0000, v188
	v_lshlrev_b32_e32 v137, 16, v189
	v_and_b32_e32 v125, 0xffff0000, v189
	v_lshlrev_b32_e32 v140, 16, v190
	v_and_b32_e32 v126, 0xffff0000, v190
	v_mul_f32_e32 v119, v119, v127
	v_mul_f32_e32 v3, v120, v3
	v_mul_f32_e32 v120, v121, v124
	v_mul_f32_e32 v121, v122, v137
	v_mul_f32_e32 v122, v123, v125
	v_mul_f32_e32 v123, v116, v140
	v_mul_f32_e32 v124, v117, v126
	v_mul_f32_e32 v125, v118, v141
	v_cvt_pk_bf16_f32 v116, v3, v120
	v_cvt_pk_bf16_f32 v117, v121, v122
	v_cvt_pk_bf16_f32 v118, v123, v124
	v_cvt_pk_bf16_f32 v119, v125, v119
	global_store_dwordx4 v[130:131], v[116:119], off
	s_nop 0
	v_lshl_add_u64 v[120:121], s[16:17], 0, v[128:129]
	v_or_b32_e32 v128, 0x100, v128
	v_lshl_add_u64 v[122:123], s[12:13], 0, v[128:129]
	s_nop 0
	s_waitcnt vmcnt(15)
; DI unsigned cvt_pk_bf16(float lo, float hi) { unsigned r; asm volatile("v_cvt_pk_bf16_f32 %0, %1, %2" : "=v"(r) : "v"(lo), "v"(hi)); return r; }
;     DI void operator()(const f32x4 (&acc)[2][2][4][2], const pg8::Unit& u, int wr, int wc, int fr, int fq) const {
;         const int row0 = u.pm * 256 + wr * 64 + fr, col0 = u.pn * 256 + wc * 32 + 8 * fq;
; #pragma unroll
;         for (int ai = 0; ai < 2; ++ai)
; #pragma unroll
;             for (int m = 0; m < 4; ++m)
; #pragma unroll
;                 for (int bj = 0; bj < 2; ++bj) {
;                     const size_t o = (size_t)(row0 + ai * 128 + m * 16) * D + col0 + bj * 128;
;                     const u32x4 gt = *(const u32x4*)(ga + o);
;                     float v[8];
; #pragma unroll
;                     for (int e = 0; e < 4; ++e) { v[e] = acc[ai][bj][m][0][e]; v[4 + e] = acc[ai][bj][m][1][e]; }
;                     v[0] *= bflo(gt.x); v[1] *= bfhi(gt.x); v[2] *= bflo(gt.y); v[3] *= bfhi(gt.y); v[4] *= bflo(gt.z); v[5] *= bfhi(gt.z); v[6] *= bflo(gt.w); v[7] *= bfhi(gt.w);
;                     u32x4 w; w.x = pg8::cvt_pk_bf16(v[0], v[1]); w.y = pg8::cvt_pk_bf16(v[2], v[3]); w.z = pg8::cvt_pk_bf16(v[4], v[5]); w.w = pg8::cvt_pk_bf16(v[6], v[7]);
;                     *(u32x4*)(outp + o) = w;
;                 }
;     }
	v_lshlrev_b32_e32 v126, 16, v195
	v_and_b32_e32 v119, 0xffff0000, v195
	v_lshlrev_b32_e32 v3, 16, v192
	v_and_b32_e32 v116, 0xffff0000, v192
	v_lshlrev_b32_e32 v124, 16, v193
	v_and_b32_e32 v117, 0xffff0000, v193
	v_lshlrev_b32_e32 v125, 16, v194
	v_and_b32_e32 v118, 0xffff0000, v194
	v_mul_f32_e32 v111, v111, v119
	v_mul_f32_e32 v3, v112, v3
	v_mul_f32_e32 v112, v113, v116
	v_mul_f32_e32 v113, v114, v124
	v_mul_f32_e32 v114, v115, v117
	v_mul_f32_e32 v115, v108, v125
	v_mul_f32_e32 v116, v109, v118
	v_mul_f32_e32 v117, v110, v126
	v_cvt_pk_bf16_f32 v108, v3, v112
	v_cvt_pk_bf16_f32 v109, v113, v114
	v_cvt_pk_bf16_f32 v110, v115, v116
	v_cvt_pk_bf16_f32 v111, v117, v111
	global_store_dwordx4 v[120:121], v[108:111], off
	s_nop 0
	v_or_b32_e32 v112, 32, v136
	v_ashrrev_i32_e32 v113, 31, v112
	v_lshlrev_b64 v[112:113], 11, v[112:113]
	v_lshl_add_u64 v[112:113], v[112:113], 0, v[134:135]
	v_lshlrev_b64 v[112:113], 1, v[112:113]
	v_lshl_add_u64 v[116:117], s[16:17], 0, v[128:129]
	v_lshl_add_u64 v[114:115], s[12:13], 0, v[112:113]
	s_nop 0
	s_waitcnt vmcnt(15)
	v_lshlrev_b32_e32 v120, 16, v199
	v_and_b32_e32 v111, 0xffff0000, v199
	v_lshlrev_b32_e32 v3, 16, v196
	v_and_b32_e32 v108, 0xffff0000, v196
	v_lshlrev_b32_e32 v118, 16, v197
	v_and_b32_e32 v109, 0xffff0000, v197
	v_lshlrev_b32_e32 v119, 16, v198
	v_and_b32_e32 v110, 0xffff0000, v198
	v_mul_f32_e32 v103, v103, v111
	v_mul_f32_e32 v3, v104, v3
	v_mul_f32_e32 v104, v105, v108
	v_mul_f32_e32 v105, v106, v118
	v_mul_f32_e32 v106, v107, v109
	v_mul_f32_e32 v107, v100, v119
	v_mul_f32_e32 v108, v101, v110
	v_mul_f32_e32 v109, v102, v120
	v_cvt_pk_bf16_f32 v100, v3, v104
	v_cvt_pk_bf16_f32 v101, v105, v106
	v_cvt_pk_bf16_f32 v102, v107, v108
	v_cvt_pk_bf16_f32 v103, v109, v103
	global_store_dwordx4 v[116:117], v[100:103], off
	s_nop 0
	v_lshl_add_u64 v[104:105], s[16:17], 0, v[112:113]
	v_or_b32_e32 v112, 0x100, v112
	v_lshl_add_u64 v[106:107], s[12:13], 0, v[112:113]
	s_nop 0
	s_waitcnt vmcnt(15)
	v_lshlrev_b32_e32 v110, 16, v203
	v_and_b32_e32 v103, 0xffff0000, v203
	v_lshlrev_b32_e32 v3, 16, v200
	v_and_b32_e32 v100, 0xffff0000, v200
	v_lshlrev_b32_e32 v108, 16, v201
	v_and_b32_e32 v101, 0xffff0000, v201
	v_lshlrev_b32_e32 v109, 16, v202
	v_and_b32_e32 v102, 0xffff0000, v202
	v_mul_f32_e32 v95, v95, v103
	v_mul_f32_e32 v3, v96, v3
	v_mul_f32_e32 v96, v97, v100
	v_mul_f32_e32 v97, v98, v108
	v_mul_f32_e32 v98, v99, v101
	v_mul_f32_e32 v99, v92, v109
	v_mul_f32_e32 v100, v93, v102
	v_mul_f32_e32 v101, v94, v110
	v_cvt_pk_bf16_f32 v92, v3, v96
	v_cvt_pk_bf16_f32 v93, v97, v98
	v_cvt_pk_bf16_f32 v94, v99, v100
	v_cvt_pk_bf16_f32 v95, v101, v95
	global_store_dwordx4 v[104:105], v[92:95], off
	s_nop 0
	v_or_b32_e32 v96, 48, v136
	v_ashrrev_i32_e32 v97, 31, v96
	v_lshlrev_b64 v[96:97], 11, v[96:97]
	v_lshl_add_u64 v[96:97], v[96:97], 0, v[134:135]
	v_lshlrev_b64 v[96:97], 1, v[96:97]
	v_lshl_add_u64 v[100:101], s[16:17], 0, v[112:113]
	v_lshl_add_u64 v[98:99], s[12:13], 0, v[96:97]
	s_nop 0
	s_waitcnt vmcnt(15)
	v_lshlrev_b32_e32 v104, 16, v207
	v_and_b32_e32 v95, 0xffff0000, v207
	v_lshlrev_b32_e32 v3, 16, v204
	v_and_b32_e32 v92, 0xffff0000, v204
	v_lshlrev_b32_e32 v102, 16, v205
	v_and_b32_e32 v93, 0xffff0000, v205
	v_lshlrev_b32_e32 v103, 16, v206
	v_and_b32_e32 v94, 0xffff0000, v206
	v_mul_f32_e32 v87, v87, v95
	v_mul_f32_e32 v3, v88, v3
	v_mul_f32_e32 v88, v89, v92
	v_mul_f32_e32 v89, v90, v102
	v_mul_f32_e32 v90, v91, v93
	v_mul_f32_e32 v91, v84, v103
	v_mul_f32_e32 v92, v85, v94
	v_mul_f32_e32 v93, v86, v104
	v_cvt_pk_bf16_f32 v84, v3, v88
	v_cvt_pk_bf16_f32 v85, v89, v90
	v_cvt_pk_bf16_f32 v86, v91, v92
	v_cvt_pk_bf16_f32 v87, v93, v87
	global_store_dwordx4 v[100:101], v[84:87], off
	s_nop 0
	v_lshl_add_u64 v[88:89], s[16:17], 0, v[96:97]
	v_or_b32_e32 v96, 0x100, v96
	v_lshl_add_u64 v[90:91], s[12:13], 0, v[96:97]
	s_nop 0
	s_waitcnt vmcnt(15)
	v_lshlrev_b32_e32 v94, 16, v211
	v_and_b32_e32 v87, 0xffff0000, v211
	v_lshlrev_b32_e32 v3, 16, v208
	v_and_b32_e32 v84, 0xffff0000, v208
	v_lshlrev_b32_e32 v92, 16, v209
	v_and_b32_e32 v85, 0xffff0000, v209
	v_lshlrev_b32_e32 v93, 16, v210
	v_and_b32_e32 v86, 0xffff0000, v210
	v_mul_f32_e32 v79, v79, v87
	v_mul_f32_e32 v3, v80, v3
	v_mul_f32_e32 v80, v81, v84
	v_mul_f32_e32 v81, v82, v92
	v_mul_f32_e32 v82, v83, v85
	v_mul_f32_e32 v83, v76, v93
	v_mul_f32_e32 v84, v77, v86
	v_mul_f32_e32 v85, v78, v94
	v_cvt_pk_bf16_f32 v76, v3, v80
	v_cvt_pk_bf16_f32 v77, v81, v82
	v_cvt_pk_bf16_f32 v78, v83, v84
	v_cvt_pk_bf16_f32 v79, v85, v79
	global_store_dwordx4 v[88:89], v[76:79], off
	s_nop 0
	v_lshl_add_u64 v[80:81], v[132:133], 0, s[28:29]
	v_lshl_add_u64 v[84:85], s[16:17], 0, v[96:97]
	v_lshl_add_u64 v[82:83], s[12:13], 0, v[80:81]
	s_nop 0
	s_waitcnt vmcnt(15)
	v_lshlrev_b32_e32 v88, 16, v215
	v_and_b32_e32 v79, 0xffff0000, v215
	v_lshlrev_b32_e32 v3, 16, v212
	v_and_b32_e32 v76, 0xffff0000, v212
	v_lshlrev_b32_e32 v86, 16, v213
	v_and_b32_e32 v77, 0xffff0000, v213
	v_lshlrev_b32_e32 v87, 16, v214
	v_and_b32_e32 v78, 0xffff0000, v214
	v_mul_f32_e32 v71, v71, v79
	v_mul_f32_e32 v3, v72, v3
	v_mul_f32_e32 v72, v73, v76
	v_mul_f32_e32 v73, v74, v86
	v_mul_f32_e32 v74, v75, v77
	v_mul_f32_e32 v75, v68, v87
	v_mul_f32_e32 v76, v69, v78
	v_mul_f32_e32 v77, v70, v88
	v_cvt_pk_bf16_f32 v68, v3, v72
	v_cvt_pk_bf16_f32 v69, v73, v74
	v_cvt_pk_bf16_f32 v70, v75, v76
	v_cvt_pk_bf16_f32 v71, v77, v71
	global_store_dwordx4 v[84:85], v[68:71], off
	s_nop 0
	v_lshl_add_u64 v[74:75], s[16:17], 0, v[80:81]
	v_lshl_add_u64 v[72:73], v[132:133], 0, s[36:37]
	v_lshl_add_u64 v[76:77], s[12:13], 0, v[72:73]
	s_nop 0
	s_waitcnt vmcnt(15)
; DI unsigned cvt_pk_bf16(float lo, float hi) { unsigned r; asm volatile("v_cvt_pk_bf16_f32 %0, %1, %2" : "=v"(r) : "v"(lo), "v"(hi)); return r; }
; #define PG8_BAR __builtin_amdgcn_s_barrier()
; template <class Epi, class Sched, bool ALIGN_EPI, bool SP2, bool GATHER>
; DI void gemm_phase(LAS unsigned char* lds, const Gemm g, const Sched& S, const Epi& E) {
;     ...
;         E(acc, cur, wr, wc, fr, fq);
;         if (!has_next) break;
; #pragma unroll
;         for (int a = 0; a < 2; ++a)
; #pragma unroll
;             for (int b = 0; b < 2; ++b)
; #pragma unroll
;                 for (int m = 0; m < 4; ++m)
; #pragma unroll
;                     for (int n = 0; n < 2; ++n) acc[a][b][m][n] = (f32x4){0.f, 0.f, 0.f, 0.f};
;         cur = nxt; cA = nA; cB = nB; ++ui;
; #pragma unroll
;         for (int h = 0; h < 2; ++h) { gC[h][0] = gN[h][0]; gC[h][1] = gN[h][1]; }
;         if constexpr (ALIGN_EPI) { if (wr == 1) PG8_BAR; }
;     }
;     DI void operator()(const f32x4 (&acc)[2][2][4][2], const pg8::Unit& u, int wr, int wc, int fr, int fq) const {
;         const int row0 = u.pm * 256 + wr * 64 + fr, col0 = u.pn * 256 + wc * 32 + 8 * fq;
; #pragma unroll
;         for (int ai = 0; ai < 2; ++ai)
; #pragma unroll
;             for (int m = 0; m < 4; ++m)
; #pragma unroll
;                 for (int bj = 0; bj < 2; ++bj) {
;                     const size_t o = (size_t)(row0 + ai * 128 + m * 16) * D + col0 + bj * 128;
;                     const u32x4 gt = *(const u32x4*)(ga + o);
;                     float v[8];
; #pragma unroll
;                     for (int e = 0; e < 4; ++e) { v[e] = acc[ai][bj][m][0][e]; v[4 + e] = acc[ai][bj][m][1][e]; }
;                     v[0] *= bflo(gt.x); v[1] *= bfhi(gt.x); v[2] *= bflo(gt.y); v[3] *= bfhi(gt.y); v[4] *= bflo(gt.z); v[5] *= bfhi(gt.z); v[6] *= bflo(gt.w); v[7] *= bfhi(gt.w);
;                     u32x4 w; w.x = pg8::cvt_pk_bf16(v[0], v[1]); w.y = pg8::cvt_pk_bf16(v[2], v[3]); w.z = pg8::cvt_pk_bf16(v[4], v[5]); w.w = pg8::cvt_pk_bf16(v[6], v[7]);
;                     *(u32x4*)(outp + o) = w;
;                 }
;     }
	v_lshlrev_b32_e32 v80, 16, v219
	v_and_b32_e32 v71, 0xffff0000, v219
	v_lshlrev_b32_e32 v3, 16, v216
	v_and_b32_e32 v68, 0xffff0000, v216
	v_lshlrev_b32_e32 v78, 16, v217
	v_and_b32_e32 v69, 0xffff0000, v217
	v_lshlrev_b32_e32 v79, 16, v218
	v_and_b32_e32 v70, 0xffff0000, v218
	v_mul_f32_e32 v63, v63, v71
	v_mul_f32_e32 v3, v64, v3
	v_mul_f32_e32 v64, v65, v68
	v_mul_f32_e32 v65, v66, v78
	v_mul_f32_e32 v66, v67, v69
	v_mul_f32_e32 v67, v60, v79
	v_mul_f32_e32 v68, v61, v70
	v_mul_f32_e32 v69, v62, v80
	v_cvt_pk_bf16_f32 v60, v3, v64
	v_cvt_pk_bf16_f32 v61, v65, v66
	v_cvt_pk_bf16_f32 v62, v67, v68
	v_cvt_pk_bf16_f32 v63, v69, v63
	global_store_dwordx4 v[74:75], v[60:63], off
	s_nop 0
	v_lshl_add_u64 v[66:67], s[16:17], 0, v[72:73]
	v_lshl_add_u64 v[64:65], v[132:133], 0, s[30:31]
	v_lshl_add_u64 v[68:69], s[12:13], 0, v[64:65]
	s_nop 0
	s_waitcnt vmcnt(15)
	v_lshlrev_b32_e32 v72, 16, v223
	v_and_b32_e32 v63, 0xffff0000, v223
	v_lshlrev_b32_e32 v3, 16, v220
	v_and_b32_e32 v60, 0xffff0000, v220
	v_lshlrev_b32_e32 v70, 16, v221
	v_and_b32_e32 v61, 0xffff0000, v221
	v_lshlrev_b32_e32 v71, 16, v222
	v_and_b32_e32 v62, 0xffff0000, v222
	v_mul_f32_e32 v55, v55, v63
	v_mul_f32_e32 v3, v56, v3
	v_mul_f32_e32 v56, v57, v60
	v_mul_f32_e32 v57, v58, v70
	v_mul_f32_e32 v58, v59, v61
	v_mul_f32_e32 v59, v52, v71
	v_mul_f32_e32 v60, v53, v62
	v_mul_f32_e32 v61, v54, v72
	v_cvt_pk_bf16_f32 v52, v3, v56
	v_cvt_pk_bf16_f32 v53, v57, v58
	v_cvt_pk_bf16_f32 v54, v59, v60
	v_cvt_pk_bf16_f32 v55, v61, v55
	global_store_dwordx4 v[66:67], v[52:55], off
	s_nop 0
	v_lshl_add_u64 v[58:59], s[16:17], 0, v[64:65]
	v_lshl_add_u64 v[56:57], v[132:133], 0, s[40:41]
	v_lshl_add_u64 v[60:61], s[12:13], 0, v[56:57]
	s_nop 0
	s_waitcnt vmcnt(15)
	v_lshlrev_b32_e32 v64, 16, v227
	v_and_b32_e32 v55, 0xffff0000, v227
	v_lshlrev_b32_e32 v3, 16, v224
	v_and_b32_e32 v52, 0xffff0000, v224
	v_lshlrev_b32_e32 v62, 16, v225
	v_and_b32_e32 v53, 0xffff0000, v225
	v_lshlrev_b32_e32 v63, 16, v226
	v_and_b32_e32 v54, 0xffff0000, v226
	v_mul_f32_e32 v47, v47, v55
	v_mul_f32_e32 v3, v48, v3
	v_mul_f32_e32 v48, v49, v52
	v_mul_f32_e32 v49, v50, v62
	v_mul_f32_e32 v50, v51, v53
	v_mul_f32_e32 v51, v44, v63
	v_mul_f32_e32 v52, v45, v54
	v_mul_f32_e32 v53, v46, v64
	v_cvt_pk_bf16_f32 v44, v3, v48
	v_cvt_pk_bf16_f32 v45, v49, v50
	v_cvt_pk_bf16_f32 v46, v51, v52
	v_cvt_pk_bf16_f32 v47, v53, v47
	global_store_dwordx4 v[58:59], v[44:47], off
	s_nop 0
	v_lshl_add_u64 v[50:51], s[16:17], 0, v[56:57]
	v_lshl_add_u64 v[48:49], v[132:133], 0, s[8:9]
	v_lshl_add_u64 v[52:53], s[12:13], 0, v[48:49]
	s_nop 0
	s_waitcnt vmcnt(15)
	v_lshlrev_b32_e32 v56, 16, v231
	v_and_b32_e32 v47, 0xffff0000, v231
	v_lshlrev_b32_e32 v3, 16, v228
	v_and_b32_e32 v44, 0xffff0000, v228
	v_lshlrev_b32_e32 v54, 16, v229
	v_and_b32_e32 v45, 0xffff0000, v229
	v_lshlrev_b32_e32 v55, 16, v230
	v_and_b32_e32 v46, 0xffff0000, v230
	v_mul_f32_e32 v39, v39, v47
	v_mul_f32_e32 v3, v40, v3
	v_mul_f32_e32 v40, v41, v44
	v_mul_f32_e32 v41, v42, v54
	v_mul_f32_e32 v42, v43, v45
	v_mul_f32_e32 v43, v36, v55
	v_mul_f32_e32 v44, v37, v46
	v_mul_f32_e32 v45, v38, v56
	v_cvt_pk_bf16_f32 v36, v3, v40
	v_cvt_pk_bf16_f32 v37, v41, v42
	v_cvt_pk_bf16_f32 v38, v43, v44
	v_cvt_pk_bf16_f32 v39, v45, v39
	global_store_dwordx4 v[50:51], v[36:39], off
	s_nop 0
	v_lshl_add_u64 v[42:43], s[16:17], 0, v[48:49]
	v_lshl_add_u64 v[40:41], v[132:133], 0, s[42:43]
	v_lshl_add_u64 v[44:45], s[12:13], 0, v[40:41]
	s_nop 0
	s_waitcnt vmcnt(15)
	v_lshlrev_b32_e32 v48, 16, v235
	v_and_b32_e32 v39, 0xffff0000, v235
	v_lshlrev_b32_e32 v3, 16, v232
	v_and_b32_e32 v36, 0xffff0000, v232
	v_lshlrev_b32_e32 v46, 16, v233
	v_and_b32_e32 v37, 0xffff0000, v233
	v_lshlrev_b32_e32 v47, 16, v234
	v_and_b32_e32 v38, 0xffff0000, v234
	v_mul_f32_e32 v31, v31, v39
	v_mul_f32_e32 v3, v32, v3
	v_mul_f32_e32 v32, v33, v36
	v_mul_f32_e32 v33, v34, v46
	v_mul_f32_e32 v34, v35, v37
	v_mul_f32_e32 v35, v28, v47
	v_mul_f32_e32 v36, v29, v38
	v_mul_f32_e32 v37, v30, v48
	v_cvt_pk_bf16_f32 v28, v3, v32
	v_cvt_pk_bf16_f32 v29, v33, v34
	v_cvt_pk_bf16_f32 v30, v35, v36
	v_cvt_pk_bf16_f32 v31, v37, v31
	global_store_dwordx4 v[42:43], v[28:31], off
	s_nop 0
	v_lshl_add_u64 v[34:35], s[16:17], 0, v[40:41]
	v_lshl_add_u64 v[32:33], v[132:133], 0, s[34:35]
	v_lshl_add_u64 v[36:37], s[12:13], 0, v[32:33]
	s_nop 0
	s_waitcnt vmcnt(15)
	v_lshlrev_b32_e32 v40, 16, v239
	v_and_b32_e32 v31, 0xffff0000, v239
	v_lshlrev_b32_e32 v3, 16, v236
	v_and_b32_e32 v28, 0xffff0000, v236
	v_lshlrev_b32_e32 v38, 16, v237
	v_and_b32_e32 v29, 0xffff0000, v237
	v_lshlrev_b32_e32 v39, 16, v238
	v_and_b32_e32 v30, 0xffff0000, v238
	v_mul_f32_e32 v23, v23, v31
	v_mul_f32_e32 v3, v24, v3
	v_mul_f32_e32 v24, v25, v28
	v_mul_f32_e32 v25, v26, v38
	v_mul_f32_e32 v26, v27, v29
	v_mul_f32_e32 v27, v20, v39
	v_mul_f32_e32 v28, v21, v30
	v_mul_f32_e32 v29, v22, v40
	v_cvt_pk_bf16_f32 v20, v3, v24
	v_cvt_pk_bf16_f32 v21, v25, v26
	v_cvt_pk_bf16_f32 v22, v27, v28
	v_cvt_pk_bf16_f32 v23, v29, v23
	global_store_dwordx4 v[34:35], v[20:23], off
	s_nop 0
	v_lshl_add_u64 v[26:27], s[16:17], 0, v[32:33]
	v_lshl_add_u64 v[24:25], v[132:133], 0, s[44:45]
	v_lshl_add_u64 v[28:29], s[12:13], 0, v[24:25]
	s_nop 0
	s_waitcnt vmcnt(15)
	v_lshlrev_b32_e32 v32, 16, v243
	v_and_b32_e32 v23, 0xffff0000, v243
	v_lshlrev_b32_e32 v3, 16, v240
	v_and_b32_e32 v20, 0xffff0000, v240
	v_lshlrev_b32_e32 v30, 16, v241
	v_and_b32_e32 v21, 0xffff0000, v241
	v_lshlrev_b32_e32 v31, 16, v242
	v_and_b32_e32 v22, 0xffff0000, v242
	v_mul_f32_e32 v15, v15, v23
	v_mul_f32_e32 v3, v16, v3
	v_mul_f32_e32 v16, v17, v20
	v_mul_f32_e32 v17, v18, v30
	v_mul_f32_e32 v18, v19, v21
	v_mul_f32_e32 v19, v12, v31
	v_mul_f32_e32 v20, v13, v22
	v_mul_f32_e32 v21, v14, v32
	v_cvt_pk_bf16_f32 v12, v3, v16
	v_cvt_pk_bf16_f32 v13, v17, v18
	v_cvt_pk_bf16_f32 v14, v19, v20
	v_cvt_pk_bf16_f32 v15, v21, v15
	global_store_dwordx4 v[26:27], v[12:15], off
	s_nop 0
	v_lshl_add_u64 v[16:17], s[16:17], 0, v[24:25]
	s_nop 0
	s_waitcnt vmcnt(15)
	v_lshlrev_b32_e32 v20, 16, v247
	v_and_b32_e32 v15, 0xffff0000, v247
	v_lshlrev_b32_e32 v3, 16, v244
	v_and_b32_e32 v12, 0xffff0000, v244
	v_lshlrev_b32_e32 v18, 16, v245
	v_and_b32_e32 v13, 0xffff0000, v245
	v_lshlrev_b32_e32 v19, 16, v246
	v_and_b32_e32 v14, 0xffff0000, v246
	v_mul_f32_e32 v7, v7, v15
	v_mul_f32_e32 v3, v8, v3
	v_mul_f32_e32 v8, v9, v12
	v_mul_f32_e32 v9, v10, v18
	v_mul_f32_e32 v10, v11, v13
	v_mul_f32_e32 v11, v4, v19
	v_mul_f32_e32 v12, v5, v14
	v_mul_f32_e32 v13, v6, v20
	v_cvt_pk_bf16_f32 v4, v3, v8
	v_cvt_pk_bf16_f32 v5, v9, v10
	v_cvt_pk_bf16_f32 v6, v11, v12
	v_cvt_pk_bf16_f32 v7, v13, v7
	global_store_dwordx4 v[16:17], v[4:7], off
	s_cbranch_vccnz .LBB0_589
	s_andn2_b64 vcc, exec, s[10:11]
	s_cbranch_vccnz .LBB0_588
	s_barrier
	s_branch .LBB0_588

; DI unsigned cvt_pk_bf16(float lo, float hi) { unsigned r; asm volatile("v_cvt_pk_bf16_f32 %0, %1, %2" : "=v"(r) : "v"(lo), "v"(hi)); return r; }
;     DI void operator()(const f32x4 (&acc)[2][2][4][2], const pg8::Unit& u, int wr, int wc, int fr, int fq) const {
;         const int row0 = u.pm * 256 + wr * 64 + fr, col0 = u.pn * 256 + wc * 32 + 8 * fq;
; #pragma unroll
;         for (int ai = 0; ai < 2; ++ai)
; #pragma unroll
;             for (int m = 0; m < 4; ++m)
; #pragma unroll
;                 for (int bj = 0; bj < 2; ++bj) {
;                     const size_t o = (size_t)(row0 + ai * 128 + m * 16) * D + col0 + bj * 128;
;                     const f32x4 a0 = *(const f32x4*)(x + o) + acc[ai][bj][m][0], a1 = *(const f32x4*)(x + o + 4) + acc[ai][bj][m][1];
;                     u32x4 w; w.x = pg8::cvt_pk_bf16(a0[0], a0[1]); w.y = pg8::cvt_pk_bf16(a0[2], a0[3]); w.z = pg8::cvt_pk_bf16(a1[0], a1[1]); w.w = pg8::cvt_pk_bf16(a1[2], a1[3]);
;                     *(u32x4*)(x1b + o) = w;
;                 }
;     }
.LBB0_677:
	v_lshl_add_u32 v172, s34, 8, v1
	v_lshl_or_b32 v174, s56, 8, v153
	v_ashrrev_i32_e32 v173, 31, v172
	v_ashrrev_i32_e32 v175, 31, v174
	v_lshlrev_b64 v[240:241], 11, v[172:173]
	v_lshl_add_u64 v[242:243], v[240:241], 0, v[174:175]
	v_lshl_add_u64 v[240:241], v[242:243], 2, s[6:7]
	global_load_dwordx4 v[176:179], v[240:241], off
	global_load_dwordx4 v[180:183], v[240:241], off offset:16
	global_load_dwordx4 v[184:187], v[240:241], off offset:512
	global_load_dwordx4 v[188:191], v[240:241], off offset:528
	v_or_b32_e32 v240, 16, v172
	v_ashrrev_i32_e32 v241, 31, v240
	v_lshlrev_b64 v[242:243], 11, v[240:241]
	v_lshl_add_u64 v[240:241], v[242:243], 0, v[174:175]
	v_lshl_add_u64 v[242:243], v[240:241], 2, s[6:7]
	global_load_dwordx4 v[192:195], v[242:243], off
	global_load_dwordx4 v[196:199], v[242:243], off offset:16
	global_load_dwordx4 v[200:203], v[242:243], off offset:512
	global_load_dwordx4 v[204:207], v[242:243], off offset:528
	v_or_b32_e32 v240, 32, v172
	v_ashrrev_i32_e32 v241, 31, v240
	v_lshlrev_b64 v[242:243], 11, v[240:241]
	v_lshl_add_u64 v[240:241], v[242:243], 0, v[174:175]
	v_lshl_add_u64 v[242:243], v[240:241], 2, s[6:7]
	global_load_dwordx4 v[208:211], v[242:243], off
	global_load_dwordx4 v[212:215], v[242:243], off offset:16
	global_load_dwordx4 v[216:219], v[242:243], off offset:512
	global_load_dwordx4 v[220:223], v[242:243], off offset:528
	v_or_b32_e32 v240, 48, v172
	v_ashrrev_i32_e32 v241, 31, v240
	v_lshlrev_b64 v[172:173], 11, v[240:241]
	v_lshl_add_u64 v[240:241], v[172:173], 0, v[174:175]
	v_lshl_add_u64 v[172:173], v[240:241], 2, s[6:7]
	global_load_dwordx4 v[224:227], v[172:173], off
	global_load_dwordx4 v[228:231], v[172:173], off offset:16
	global_load_dwordx4 v[232:235], v[172:173], off offset:512
	global_load_dwordx4 v[236:239], v[172:173], off offset:528
	v_lshl_add_u32 v150, s34, 8, v1
	v_lshl_or_b32 v148, s56, 8, v153
	v_ashrrev_i32_e32 v151, 31, v150
	v_ashrrev_i32_e32 v149, 31, v148
	v_lshlrev_b64 v[146:147], 11, v[150:151]
	v_lshl_add_u64 v[146:147], v[146:147], 0, v[148:149]
	v_lshl_add_u64 v[166:167], v[146:147], 2, s[6:7]
	s_nop 0
	s_nop 0
	v_lshlrev_b64 v[168:169], 1, v[146:147]
	v_lshl_add_u64 v[170:171], s[10:11], 0, v[168:169]
	v_or_b32_e32 v168, 0x100, v168
	s_andn2_b64 vcc, exec, s[4:5]
	s_mov_b64 s[4:5], -1
	s_nop 0
	s_waitcnt vmcnt(15)
	v_pk_add_f32 v[126:127], v[126:127], v[176:177]
	s_waitcnt vmcnt(14)
	v_pk_add_f32 v[158:159], v[124:125], v[182:183]
	v_pk_add_f32 v[124:125], v[122:123], v[180:181]
	v_pk_add_f32 v[128:129], v[128:129], v[178:179]
	v_cvt_pk_bf16_f32 v122, v126, v127
	v_lshl_add_u64 v[162:163], s[10:11], 0, v[168:169]
	v_cvt_pk_bf16_f32 v123, v128, v129
	v_cvt_pk_bf16_f32 v124, v124, v125
	v_cvt_pk_bf16_f32 v125, v158, v159
	global_store_dwordx4 v[170:171], v[122:125], off
	s_nop 0
	s_nop 0
	s_nop 0
	v_or_b32_e32 v158, 16, v150
	v_ashrrev_i32_e32 v159, 31, v158
	v_lshlrev_b64 v[158:159], 11, v[158:159]
	v_lshl_add_u64 v[158:159], v[158:159], 0, v[148:149]
	v_lshl_add_u64 v[160:161], v[158:159], 2, s[6:7]
	s_nop 0
	s_waitcnt vmcnt(14)
	v_pk_add_f32 v[118:119], v[118:119], v[184:185]
	s_nop 0
	s_waitcnt vmcnt(13)
	v_pk_add_f32 v[122:123], v[116:117], v[190:191]
	v_pk_add_f32 v[116:117], v[114:115], v[188:189]
	v_pk_add_f32 v[120:121], v[120:121], v[186:187]
	v_cvt_pk_bf16_f32 v114, v118, v119
	s_nop 0
	v_cvt_pk_bf16_f32 v115, v120, v121
	v_cvt_pk_bf16_f32 v116, v116, v117
	v_cvt_pk_bf16_f32 v117, v122, v123
	global_store_dwordx4 v[162:163], v[114:117], off
	s_nop 0
	s_nop 0
	s_nop 0
	v_lshlrev_b64 v[122:123], 1, v[158:159]
	v_lshl_add_u64 v[124:125], s[10:11], 0, v[122:123]
	v_or_b32_e32 v122, 0x100, v122
	s_nop 0
	s_waitcnt vmcnt(13)
	v_pk_add_f32 v[110:111], v[110:111], v[192:193]
	s_nop 0
	s_waitcnt vmcnt(12)
	v_pk_add_f32 v[114:115], v[108:109], v[198:199]
	v_pk_add_f32 v[108:109], v[106:107], v[196:197]
	v_pk_add_f32 v[112:113], v[112:113], v[194:195]
	v_cvt_pk_bf16_f32 v106, v110, v111
	v_lshl_add_u64 v[118:119], s[10:11], 0, v[122:123]
	v_cvt_pk_bf16_f32 v107, v112, v113
	v_cvt_pk_bf16_f32 v108, v108, v109
	v_cvt_pk_bf16_f32 v109, v114, v115
	global_store_dwordx4 v[124:125], v[106:109], off
	s_nop 0
	s_nop 0
	s_nop 0
	v_or_b32_e32 v114, 32, v150
	v_ashrrev_i32_e32 v115, 31, v114
	v_lshlrev_b64 v[114:115], 11, v[114:115]
	v_lshl_add_u64 v[114:115], v[114:115], 0, v[148:149]
	v_lshl_add_u64 v[116:117], v[114:115], 2, s[6:7]
	s_nop 0
	s_waitcnt vmcnt(12)
	v_pk_add_f32 v[102:103], v[102:103], v[200:201]
	s_nop 0
	s_waitcnt vmcnt(11)
	v_pk_add_f32 v[106:107], v[100:101], v[206:207]
	v_pk_add_f32 v[100:101], v[98:99], v[204:205]
	v_pk_add_f32 v[104:105], v[104:105], v[202:203]
	v_cvt_pk_bf16_f32 v98, v102, v103
	s_nop 0
	v_cvt_pk_bf16_f32 v99, v104, v105
	v_cvt_pk_bf16_f32 v100, v100, v101
	v_cvt_pk_bf16_f32 v101, v106, v107
	global_store_dwordx4 v[118:119], v[98:101], off
	s_nop 0
	s_nop 0
	s_nop 0
	v_lshlrev_b64 v[106:107], 1, v[114:115]
	v_lshl_add_u64 v[108:109], s[10:11], 0, v[106:107]
	v_or_b32_e32 v106, 0x100, v106
	s_nop 0
	s_waitcnt vmcnt(11)
	v_pk_add_f32 v[94:95], v[94:95], v[208:209]
	s_nop 0
	s_waitcnt vmcnt(10)
	v_pk_add_f32 v[98:99], v[92:93], v[214:215]
	v_pk_add_f32 v[92:93], v[90:91], v[212:213]
	v_pk_add_f32 v[96:97], v[96:97], v[210:211]
	v_cvt_pk_bf16_f32 v90, v94, v95
	v_lshl_add_u64 v[102:103], s[10:11], 0, v[106:107]
	v_cvt_pk_bf16_f32 v91, v96, v97
	v_cvt_pk_bf16_f32 v92, v92, v93
	v_cvt_pk_bf16_f32 v93, v98, v99
	global_store_dwordx4 v[108:109], v[90:93], off
	s_nop 0
	s_nop 0
	s_nop 0
	v_or_b32_e32 v98, 48, v150
	v_ashrrev_i32_e32 v99, 31, v98
	v_lshlrev_b64 v[98:99], 11, v[98:99]
	v_lshl_add_u64 v[98:99], v[98:99], 0, v[148:149]
	v_lshl_add_u64 v[100:101], v[98:99], 2, s[6:7]
	s_nop 0
	s_waitcnt vmcnt(10)
; DI unsigned cvt_pk_bf16(float lo, float hi) { unsigned r; asm volatile("v_cvt_pk_bf16_f32 %0, %1, %2" : "=v"(r) : "v"(lo), "v"(hi)); return r; }
;     DI void operator()(const f32x4 (&acc)[2][2][4][2], const pg8::Unit& u, int wr, int wc, int fr, int fq) const {
;         const int row0 = u.pm * 256 + wr * 64 + fr, col0 = u.pn * 256 + wc * 32 + 8 * fq;
; #pragma unroll
;         for (int ai = 0; ai < 2; ++ai)
; #pragma unroll
;             for (int m = 0; m < 4; ++m)
; #pragma unroll
;                 for (int bj = 0; bj < 2; ++bj) {
;                     const size_t o = (size_t)(row0 + ai * 128 + m * 16) * D + col0 + bj * 128;
;                     const f32x4 a0 = *(const f32x4*)(x + o) + acc[ai][bj][m][0], a1 = *(const f32x4*)(x + o + 4) + acc[ai][bj][m][1];
;                     u32x4 w; w.x = pg8::cvt_pk_bf16(a0[0], a0[1]); w.y = pg8::cvt_pk_bf16(a0[2], a0[3]); w.z = pg8::cvt_pk_bf16(a1[0], a1[1]); w.w = pg8::cvt_pk_bf16(a1[2], a1[3]);
;                     *(u32x4*)(x1b + o) = w;
;                 }
;     }
	v_pk_add_f32 v[86:87], v[86:87], v[216:217]
	s_nop 0
	s_waitcnt vmcnt(9)
	v_pk_add_f32 v[90:91], v[84:85], v[222:223]
	v_pk_add_f32 v[84:85], v[82:83], v[220:221]
	v_pk_add_f32 v[88:89], v[88:89], v[218:219]
	v_cvt_pk_bf16_f32 v82, v86, v87
	s_nop 0
	v_cvt_pk_bf16_f32 v83, v88, v89
	v_cvt_pk_bf16_f32 v84, v84, v85
	v_cvt_pk_bf16_f32 v85, v90, v91
	global_store_dwordx4 v[102:103], v[82:85], off
	s_nop 0
	s_nop 0
	s_nop 0
	v_lshlrev_b64 v[90:91], 1, v[98:99]
	v_lshl_add_u64 v[92:93], s[10:11], 0, v[90:91]
	v_or_b32_e32 v90, 0x100, v90
	s_nop 0
	s_waitcnt vmcnt(9)
	v_pk_add_f32 v[78:79], v[78:79], v[224:225]
	s_nop 0
	s_waitcnt vmcnt(8)
	v_pk_add_f32 v[82:83], v[76:77], v[230:231]
	v_pk_add_f32 v[76:77], v[74:75], v[228:229]
	v_pk_add_f32 v[80:81], v[80:81], v[226:227]
	v_cvt_pk_bf16_f32 v74, v78, v79
	v_lshl_add_u64 v[86:87], s[10:11], 0, v[90:91]
	v_cvt_pk_bf16_f32 v75, v80, v81
	v_cvt_pk_bf16_f32 v76, v76, v77
	v_cvt_pk_bf16_f32 v77, v82, v83
	global_store_dwordx4 v[92:93], v[74:77], off
	s_nop 0
	s_nop 0
	s_nop 0
	v_lshl_add_u64 v[82:83], v[146:147], 0, s[16:17]
	v_lshl_add_u64 v[84:85], v[82:83], 2, s[6:7]
	s_nop 0
	s_waitcnt vmcnt(8)
	v_pk_add_f32 v[70:71], v[70:71], v[232:233]
	s_nop 0
	s_waitcnt vmcnt(7)
	v_pk_add_f32 v[74:75], v[68:69], v[238:239]
	v_pk_add_f32 v[68:69], v[66:67], v[236:237]
	v_pk_add_f32 v[72:73], v[72:73], v[234:235]
	v_cvt_pk_bf16_f32 v66, v70, v71
	s_nop 0
	v_cvt_pk_bf16_f32 v67, v72, v73
	v_cvt_pk_bf16_f32 v68, v68, v69
	v_cvt_pk_bf16_f32 v69, v74, v75
	global_store_dwordx4 v[86:87], v[66:69], off
	global_load_dwordx4 v[176:179], v[84:85], off
	global_load_dwordx4 v[180:183], v[84:85], off offset:16
	global_load_dwordx4 v[184:187], v[84:85], off offset:512
	global_load_dwordx4 v[188:191], v[84:85], off offset:528
	v_lshl_add_u64 v[172:173], v[146:147], 0, s[18:19]
	v_lshl_add_u64 v[174:175], v[172:173], 2, s[6:7]
	global_load_dwordx4 v[192:195], v[174:175], off
	global_load_dwordx4 v[196:199], v[174:175], off offset:16
	global_load_dwordx4 v[200:203], v[174:175], off offset:512
	global_load_dwordx4 v[204:207], v[174:175], off offset:528
	v_lshl_add_u64 v[172:173], v[146:147], 0, s[20:21]
	v_lshl_add_u64 v[174:175], v[172:173], 2, s[6:7]
	global_load_dwordx4 v[208:211], v[174:175], off
	global_load_dwordx4 v[212:215], v[174:175], off offset:16
	global_load_dwordx4 v[216:219], v[174:175], off offset:512
	global_load_dwordx4 v[220:223], v[174:175], off offset:528
	v_lshl_add_u64 v[172:173], v[146:147], 0, s[22:23]
	v_lshl_add_u64 v[174:175], v[172:173], 2, s[6:7]
	global_load_dwordx4 v[224:227], v[174:175], off
	global_load_dwordx4 v[228:231], v[174:175], off offset:16
	global_load_dwordx4 v[232:235], v[174:175], off offset:512
	global_load_dwordx4 v[236:239], v[174:175], off offset:528
	s_nop 0
	s_nop 0
	s_nop 0
	v_lshlrev_b64 v[74:75], 1, v[82:83]
	v_lshl_add_u64 v[76:77], s[10:11], 0, v[74:75]
	v_or_b32_e32 v74, 0x100, v74
	s_nop 0
	s_waitcnt vmcnt(15)
	v_pk_add_f32 v[62:63], v[62:63], v[176:177]
	s_nop 0
	s_waitcnt vmcnt(14)
	v_pk_add_f32 v[66:67], v[60:61], v[182:183]
	v_pk_add_f32 v[60:61], v[58:59], v[180:181]
	v_pk_add_f32 v[64:65], v[64:65], v[178:179]
	v_cvt_pk_bf16_f32 v58, v62, v63
	v_lshl_add_u64 v[70:71], s[10:11], 0, v[74:75]
	v_cvt_pk_bf16_f32 v59, v64, v65
	v_cvt_pk_bf16_f32 v60, v60, v61
	v_cvt_pk_bf16_f32 v61, v66, v67
	global_store_dwordx4 v[76:77], v[58:61], off
	s_nop 0
	s_nop 0
	s_nop 0
	v_lshl_add_u64 v[66:67], v[146:147], 0, s[18:19]
	v_lshl_add_u64 v[68:69], v[66:67], 2, s[6:7]
	s_nop 0
	s_waitcnt vmcnt(14)
	v_pk_add_f32 v[54:55], v[54:55], v[184:185]
	s_nop 0
	s_waitcnt vmcnt(13)
; DI unsigned cvt_pk_bf16(float lo, float hi) { unsigned r; asm volatile("v_cvt_pk_bf16_f32 %0, %1, %2" : "=v"(r) : "v"(lo), "v"(hi)); return r; }
; #define PG8_BAR __builtin_amdgcn_s_barrier()
; template <class Epi, class Sched, bool ALIGN_EPI, bool SP2, bool GATHER>
; DI void gemm_phase(LAS unsigned char* lds, const Gemm g, const Sched& S, const Epi& E) {
;     ...
;         E(acc, cur, wr, wc, fr, fq);
;         if (!has_next) break;
; #pragma unroll
;         for (int a = 0; a < 2; ++a)
; #pragma unroll
;             for (int b = 0; b < 2; ++b)
; #pragma unroll
;                 for (int m = 0; m < 4; ++m)
; #pragma unroll
;                     for (int n = 0; n < 2; ++n) acc[a][b][m][n] = (f32x4){0.f, 0.f, 0.f, 0.f};
;         cur = nxt; cA = nA; cB = nB; ++ui;
; #pragma unroll
;         for (int h = 0; h < 2; ++h) { gC[h][0] = gN[h][0]; gC[h][1] = gN[h][1]; }
;         if constexpr (ALIGN_EPI) { if (wr == 1) PG8_BAR; }
;     }
;     DI void operator()(const f32x4 (&acc)[2][2][4][2], const pg8::Unit& u, int wr, int wc, int fr, int fq) const {
;         const int row0 = u.pm * 256 + wr * 64 + fr, col0 = u.pn * 256 + wc * 32 + 8 * fq;
; #pragma unroll
;         for (int ai = 0; ai < 2; ++ai)
; #pragma unroll
;             for (int m = 0; m < 4; ++m)
; #pragma unroll
;                 for (int bj = 0; bj < 2; ++bj) {
;                     const size_t o = (size_t)(row0 + ai * 128 + m * 16) * D + col0 + bj * 128;
;                     const f32x4 a0 = *(const f32x4*)(x + o) + acc[ai][bj][m][0], a1 = *(const f32x4*)(x + o + 4) + acc[ai][bj][m][1];
;                     u32x4 w; w.x = pg8::cvt_pk_bf16(a0[0], a0[1]); w.y = pg8::cvt_pk_bf16(a0[2], a0[3]); w.z = pg8::cvt_pk_bf16(a1[0], a1[1]); w.w = pg8::cvt_pk_bf16(a1[2], a1[3]);
;                     *(u32x4*)(x1b + o) = w;
;                 }
;     }
	v_pk_add_f32 v[58:59], v[52:53], v[190:191]
	v_pk_add_f32 v[52:53], v[50:51], v[188:189]
	v_pk_add_f32 v[56:57], v[56:57], v[186:187]
	v_cvt_pk_bf16_f32 v50, v54, v55
	s_nop 0
	v_cvt_pk_bf16_f32 v51, v56, v57
	v_cvt_pk_bf16_f32 v52, v52, v53
	v_cvt_pk_bf16_f32 v53, v58, v59
	global_store_dwordx4 v[70:71], v[50:53], off
	s_nop 0
	s_nop 0
	s_nop 0
	v_lshlrev_b64 v[58:59], 1, v[66:67]
	v_lshl_add_u64 v[60:61], s[10:11], 0, v[58:59]
	v_or_b32_e32 v58, 0x100, v58
	s_nop 0
	s_waitcnt vmcnt(13)
	v_pk_add_f32 v[46:47], v[46:47], v[192:193]
	s_nop 0
	s_waitcnt vmcnt(12)
	v_pk_add_f32 v[50:51], v[44:45], v[198:199]
	v_pk_add_f32 v[44:45], v[42:43], v[196:197]
	v_pk_add_f32 v[48:49], v[48:49], v[194:195]
	v_cvt_pk_bf16_f32 v42, v46, v47
	v_lshl_add_u64 v[54:55], s[10:11], 0, v[58:59]
	v_cvt_pk_bf16_f32 v43, v48, v49
	v_cvt_pk_bf16_f32 v44, v44, v45
	v_cvt_pk_bf16_f32 v45, v50, v51
	global_store_dwordx4 v[60:61], v[42:45], off
	s_nop 0
	s_nop 0
	s_nop 0
	v_lshl_add_u64 v[50:51], v[146:147], 0, s[20:21]
	v_lshl_add_u64 v[52:53], v[50:51], 2, s[6:7]
	s_nop 0
	s_waitcnt vmcnt(12)
	v_pk_add_f32 v[30:31], v[30:31], v[200:201]
	s_nop 0
	s_waitcnt vmcnt(11)
	v_pk_add_f32 v[42:43], v[28:29], v[206:207]
	v_pk_add_f32 v[28:29], v[26:27], v[204:205]
	v_pk_add_f32 v[32:33], v[32:33], v[202:203]
	v_cvt_pk_bf16_f32 v26, v30, v31
	s_nop 0
	v_cvt_pk_bf16_f32 v27, v32, v33
	v_cvt_pk_bf16_f32 v28, v28, v29
	v_cvt_pk_bf16_f32 v29, v42, v43
	global_store_dwordx4 v[54:55], v[26:29], off
	s_nop 0
	s_nop 0
	s_nop 0
	v_lshlrev_b64 v[42:43], 1, v[50:51]
	v_lshl_add_u64 v[44:45], s[10:11], 0, v[42:43]
	v_or_b32_e32 v42, 0x100, v42
	s_nop 0
	s_waitcnt vmcnt(11)
	v_pk_add_f32 v[22:23], v[22:23], v[208:209]
	s_nop 0
	s_waitcnt vmcnt(10)
	v_pk_add_f32 v[26:27], v[20:21], v[214:215]
	v_pk_add_f32 v[20:21], v[18:19], v[212:213]
	v_pk_add_f32 v[24:25], v[24:25], v[210:211]
	v_cvt_pk_bf16_f32 v18, v22, v23
	v_lshl_add_u64 v[30:31], s[10:11], 0, v[42:43]
	v_cvt_pk_bf16_f32 v19, v24, v25
	v_cvt_pk_bf16_f32 v20, v20, v21
	v_cvt_pk_bf16_f32 v21, v26, v27
	global_store_dwordx4 v[44:45], v[18:21], off
	s_nop 0
	s_nop 0
	s_nop 0
	v_lshl_add_u64 v[26:27], v[146:147], 0, s[22:23]
	v_lshl_add_u64 v[28:29], v[26:27], 2, s[6:7]
	v_lshlrev_b64 v[26:27], 1, v[26:27]
	s_nop 0
	s_waitcnt vmcnt(10)
	v_pk_add_f32 v[20:21], v[36:37], v[218:219]
	v_pk_add_f32 v[18:19], v[34:35], v[216:217]
	s_nop 0
	s_waitcnt vmcnt(9)
	v_pk_add_f32 v[24:25], v[40:41], v[222:223]
	v_pk_add_f32 v[22:23], v[38:39], v[220:221]
	v_cvt_pk_bf16_f32 v18, v18, v19
	v_cvt_pk_bf16_f32 v19, v20, v21
	s_nop 0
	v_cvt_pk_bf16_f32 v20, v22, v23
	v_cvt_pk_bf16_f32 v21, v24, v25
	global_store_dwordx4 v[30:31], v[18:21], off
	s_nop 0
	s_nop 0
	s_nop 0
	v_lshl_add_u64 v[30:31], s[10:11], 0, v[26:27]
	v_or_b32_e32 v26, 0x100, v26
	s_nop 0
	s_waitcnt vmcnt(9)
	v_pk_add_f32 v[6:7], v[6:7], v[224:225]
	s_nop 0
	s_waitcnt vmcnt(8)
	v_pk_add_f32 v[18:19], v[4:5], v[230:231]
	v_pk_add_f32 v[4:5], v[2:3], v[228:229]
	v_pk_add_f32 v[8:9], v[8:9], v[226:227]
	v_cvt_pk_bf16_f32 v2, v6, v7
	s_nop 0
	v_cvt_pk_bf16_f32 v3, v8, v9
	v_cvt_pk_bf16_f32 v4, v4, v5
	v_cvt_pk_bf16_f32 v5, v18, v19
	global_store_dwordx4 v[30:31], v[2:5], off
	s_nop 0
	s_nop 0
	s_nop 0
	v_lshl_add_u64 v[18:19], s[10:11], 0, v[26:27]
	s_nop 0
	s_waitcnt vmcnt(8)
	v_pk_add_f32 v[4:5], v[12:13], v[234:235]
	v_pk_add_f32 v[2:3], v[10:11], v[232:233]
	s_nop 0
	s_waitcnt vmcnt(7)
	v_pk_add_f32 v[8:9], v[16:17], v[238:239]
	v_pk_add_f32 v[6:7], v[14:15], v[236:237]
	v_cvt_pk_bf16_f32 v2, v2, v3
	v_cvt_pk_bf16_f32 v3, v4, v5
	s_nop 0
	v_cvt_pk_bf16_f32 v4, v6, v7
	v_cvt_pk_bf16_f32 v5, v8, v9
	global_store_dwordx4 v[18:19], v[2:5], off
	s_cbranch_vccnz .LBB0_666
	s_andn2_b64 vcc, exec, s[8:9]
	s_cbranch_vccnz .LBB0_665
	s_barrier
	s_branch .LBB0_665

; DI float sigmoidf_(float x) { return __builtin_amdgcn_rcpf(1.0f + __expf(-x)); }
; DI unsigned cvt_pk_bf16(float lo, float hi) { unsigned r; asm volatile("v_cvt_pk_bf16_f32 %0, %1, %2" : "=v"(r) : "v"(lo), "v"(hi)); return r; }
;     DI void operator()(const f32x4 (&acc)[2][2][4][2], const pg8::Unit& u, int wr, int wc, int fr, int fq) const {
;         const int row0 = u.pm * 256 + wr * 64 + fr, pnr = u.pn & 3;
; #pragma unroll
;         for (int ai = 0; ai < 2; ++ai)
; #pragma unroll
;             for (int m = 0; m < 4; ++m) {
;                 const int p = row0 + ai * 128 + m * 16; const float r = rowr2[p];
; #pragma unroll
;                 for (int bj = 0; bj < 2; ++bj) {
;                     const int f0 = 128 * pnr + 64 * bj + 16 * wc + 4 * fq;
;                     float o[4];
; #pragma unroll
;                     for (int e = 0; e < 4; ++e) { const float g = acc[ai][bj][m][0][e] * r, up = acc[ai][bj][m][1][e] * r; o[e] = g * sigmoidf_(g) * up; }
;                     u32x2 w; w.x = pg8::cvt_pk_bf16(o[0], o[1]); w.y = pg8::cvt_pk_bf16(o[2], o[3]);
;                     *(u32x2*)(U + (size_t)p * FF + f0) = w;
;                 }
;             }
;     }
.LBB0_910:
	v_lshl_add_u32 v164, s63, 8, v154
	v_ashrrev_i32_e32 v165, 31, v164
	v_lshl_add_u64 v[166:167], v[164:165], 2, s[10:11]
	global_load_dword v176, v[166:167], off
	v_or_b32_e32 v168, 16, v164
	v_ashrrev_i32_e32 v169, 31, v168
	v_lshl_add_u64 v[170:171], v[168:169], 2, s[10:11]
	global_load_dword v178, v[170:171], off
	v_or_b32_e32 v168, 32, v164
	v_ashrrev_i32_e32 v169, 31, v168
	v_lshl_add_u64 v[170:171], v[168:169], 2, s[10:11]
	global_load_dword v180, v[170:171], off
	v_or_b32_e32 v168, 48, v164
	v_ashrrev_i32_e32 v169, 31, v168
	v_lshl_add_u64 v[164:165], v[168:169], 2, s[10:11]
	global_load_dword v182, v[164:165], off
	global_load_dword v184, v[166:167], off offset:512
	global_load_dword v186, v[166:167], off offset:576
	global_load_dword v188, v[166:167], off offset:640
	global_load_dword v190, v[166:167], off offset:704
	v_lshl_add_u32 v142, s63, 8, v154
	v_ashrrev_i32_e32 v143, 31, v142
	v_lshl_add_u64 v[140:141], v[142:143], 2, s[10:11]
	s_nop 0
	v_mov_b32_e32 v146, v126
	v_mov_b32_e32 v147, v122
	v_mov_b32_e32 v122, v127
	v_mov_b32_e32 v126, v128
	v_mov_b32_e32 v127, v124
	v_mov_b32_e32 v124, v129
	v_mov_b32_e32 v129, v114
	v_mov_b32_e32 v114, v119
	v_mov_b32_e32 v128, v118
	v_mov_b32_e32 v148, v120
	v_mov_b32_e32 v149, v116
	v_mov_b32_e32 v116, v121
	v_lshlrev_b64 v[118:119], 10, v[142:143]
	s_lshl_b32 s29, s34, 7
	s_and_b32 s29, s29, 0x180
	v_or_b32_e32 v134, s29, v156
	v_or_b32_e32 v120, 16, v142
	v_lshl_add_u64 v[118:119], s[12:13], 0, v[118:119]
	v_lshlrev_b32_e32 v134, 1, v134
	v_ashrrev_i32_e32 v121, 31, v120
	v_lshl_add_u64 v[118:119], v[118:119], 0, v[134:135]
	v_lshl_add_u64 v[150:151], v[120:121], 2, s[10:11]
	v_lshlrev_b64 v[120:121], 10, v[120:121]
	v_lshl_add_u64 v[120:121], s[12:13], 0, v[120:121]
	v_lshl_add_u64 v[120:121], v[120:121], 0, v[134:135]
	s_nop 0
	s_waitcnt vmcnt(7)
	v_pk_mul_f32 v[146:147], v[146:147], v[176:177] op_sel_hi:[1,0]
	v_pk_mul_f32 v[122:123], v[122:123], v[176:177] op_sel_hi:[1,0]
	v_pk_mul_f32 v[126:127], v[126:127], v[176:177] op_sel_hi:[1,0]
	v_pk_mul_f32 v[124:125], v[124:125], v[176:177] op_sel_hi:[1,0]
	v_pk_mul_f32 v[114:115], v[114:115], v[176:177] op_sel_hi:[1,0]
	v_pk_mul_f32 v[128:129], v[128:129], v[176:177] op_sel_hi:[1,0]
	v_pk_mul_f32 v[148:149], v[148:149], v[176:177] op_sel_hi:[1,0]
	v_pk_mul_f32 v[116:117], v[116:117], v[176:177] op_sel_hi:[1,0]
	v_mul_f32_e32 v137, 0xbfb8aa3b, v147
	v_mul_f32_e32 v139, 0xbfb8aa3b, v123
	v_mul_f32_e32 v143, 0xbfb8aa3b, v127
	v_mul_f32_e32 v144, 0xbfb8aa3b, v125
	v_mul_f32_e32 v160, 0xbfb8aa3b, v115
	v_mul_f32_e32 v145, 0xbfb8aa3b, v129
	v_mul_f32_e32 v161, 0xbfb8aa3b, v149
	v_mul_f32_e32 v162, 0xbfb8aa3b, v117
	v_exp_f32_e32 v137, v137
	v_exp_f32_e32 v139, v139
	v_exp_f32_e32 v143, v143
	v_exp_f32_e32 v144, v144
	v_exp_f32_e32 v160, v160
	v_exp_f32_e32 v145, v145
	v_exp_f32_e32 v161, v161
	v_exp_f32_e32 v162, v162
	v_add_f32_e32 v137, 1.0, v137
	v_add_f32_e32 v139, 1.0, v139
	v_add_f32_e32 v143, 1.0, v143
	v_add_f32_e32 v144, 1.0, v144
	v_add_f32_e32 v160, 1.0, v160
	v_add_f32_e32 v145, 1.0, v145
	v_add_f32_e32 v161, 1.0, v161
	v_add_f32_e32 v162, 1.0, v162
	v_rcp_f32_e32 v137, v137
	v_rcp_f32_e32 v139, v139
	v_rcp_f32_e32 v143, v143
	v_rcp_f32_e32 v144, v144
	v_rcp_f32_e32 v160, v160
	v_rcp_f32_e32 v145, v145
	v_rcp_f32_e32 v161, v161
	v_rcp_f32_e32 v162, v162
	v_mul_f32_e32 v137, v147, v137
	v_mul_f32_e32 v123, v123, v139
	v_mul_f32_e32 v127, v127, v143
	v_mul_f32_e32 v125, v125, v144
	v_mul_f32_e32 v115, v115, v160
	v_mul_f32_e32 v129, v129, v145
	v_mul_f32_e32 v139, v149, v161
	v_mul_f32_e32 v117, v117, v162
	v_mul_f32_e32 v137, v146, v137
	v_mul_f32_e32 v122, v122, v123
	v_mul_f32_e32 v123, v126, v127
	v_mul_f32_e32 v124, v124, v125
	v_mul_f32_e32 v126, v114, v115
	v_cvt_pk_bf16_f32 v114, v137, v122
	v_cvt_pk_bf16_f32 v115, v123, v124
	v_mul_f32_e32 v125, v128, v129
	v_mul_f32_e32 v127, v148, v139
	v_mul_f32_e32 v116, v116, v117
	global_store_dwordx2 v[118:119], v[114:115], off
	v_cvt_pk_bf16_f32 v114, v125, v126
	v_cvt_pk_bf16_f32 v115, v127, v116
	global_store_dwordx2 v[118:119], v[114:115], off offset:128
	s_nop 0
	v_mov_b32_e32 v116, v110
	v_mov_b32_e32 v117, v106
	v_mov_b32_e32 v106, v111
	v_mov_b32_e32 v110, v112
	v_mov_b32_e32 v111, v108
	v_mov_b32_e32 v108, v113
	v_mov_b32_e32 v113, v98
	v_mov_b32_e32 v98, v103
	v_mov_b32_e32 v112, v102
	v_mov_b32_e32 v102, v104
	v_mov_b32_e32 v103, v100
	v_mov_b32_e32 v100, v105
	v_or_b32_e32 v104, 32, v142
	v_ashrrev_i32_e32 v105, 31, v104
	v_lshl_add_u64 v[122:123], v[104:105], 2, s[10:11]
	s_nop 0
	s_waitcnt vmcnt(8)
; DI float sigmoidf_(float x) { return __builtin_amdgcn_rcpf(1.0f + __expf(-x)); }
; DI unsigned cvt_pk_bf16(float lo, float hi) { unsigned r; asm volatile("v_cvt_pk_bf16_f32 %0, %1, %2" : "=v"(r) : "v"(lo), "v"(hi)); return r; }
;     DI void operator()(const f32x4 (&acc)[2][2][4][2], const pg8::Unit& u, int wr, int wc, int fr, int fq) const {
;         const int row0 = u.pm * 256 + wr * 64 + fr, pnr = u.pn & 3;
; #pragma unroll
;         for (int ai = 0; ai < 2; ++ai)
; #pragma unroll
;             for (int m = 0; m < 4; ++m) {
;                 const int p = row0 + ai * 128 + m * 16; const float r = rowr2[p];
; #pragma unroll
;                 for (int bj = 0; bj < 2; ++bj) {
;                     const int f0 = 128 * pnr + 64 * bj + 16 * wc + 4 * fq;
;                     float o[4];
; #pragma unroll
;                     for (int e = 0; e < 4; ++e) { const float g = acc[ai][bj][m][0][e] * r, up = acc[ai][bj][m][1][e] * r; o[e] = g * sigmoidf_(g) * up; }
;                     u32x2 w; w.x = pg8::cvt_pk_bf16(o[0], o[1]); w.y = pg8::cvt_pk_bf16(o[2], o[3]);
;                     *(u32x2*)(U + (size_t)p * FF + f0) = w;
;                 }
;             }
;     }
	v_pk_mul_f32 v[116:117], v[116:117], v[178:179] op_sel_hi:[1,0]
	v_pk_mul_f32 v[106:107], v[106:107], v[178:179] op_sel_hi:[1,0]
	v_pk_mul_f32 v[110:111], v[110:111], v[178:179] op_sel_hi:[1,0]
	v_pk_mul_f32 v[108:109], v[108:109], v[178:179] op_sel_hi:[1,0]
	v_pk_mul_f32 v[98:99], v[98:99], v[178:179] op_sel_hi:[1,0]
	v_pk_mul_f32 v[112:113], v[112:113], v[178:179] op_sel_hi:[1,0]
	v_pk_mul_f32 v[102:103], v[102:103], v[178:179] op_sel_hi:[1,0]
	v_pk_mul_f32 v[100:101], v[100:101], v[178:179] op_sel_hi:[1,0]
	v_mul_f32_e32 v114, 0xbfb8aa3b, v117
	v_mul_f32_e32 v115, 0xbfb8aa3b, v107
	v_mul_f32_e32 v124, 0xbfb8aa3b, v111
	v_mul_f32_e32 v125, 0xbfb8aa3b, v109
	v_mul_f32_e32 v127, 0xbfb8aa3b, v99
	v_mul_f32_e32 v126, 0xbfb8aa3b, v113
	v_mul_f32_e32 v128, 0xbfb8aa3b, v103
	v_mul_f32_e32 v129, 0xbfb8aa3b, v101
	v_exp_f32_e32 v114, v114
	v_exp_f32_e32 v115, v115
	v_exp_f32_e32 v124, v124
	v_exp_f32_e32 v125, v125
	v_exp_f32_e32 v127, v127
	v_exp_f32_e32 v126, v126
	v_exp_f32_e32 v128, v128
	v_exp_f32_e32 v129, v129
	v_add_f32_e32 v114, 1.0, v114
	v_add_f32_e32 v115, 1.0, v115
	v_add_f32_e32 v124, 1.0, v124
	v_add_f32_e32 v125, 1.0, v125
	v_add_f32_e32 v127, 1.0, v127
	v_add_f32_e32 v126, 1.0, v126
	v_add_f32_e32 v128, 1.0, v128
	v_add_f32_e32 v129, 1.0, v129
	v_rcp_f32_e32 v114, v114
	v_rcp_f32_e32 v115, v115
	v_rcp_f32_e32 v124, v124
	v_rcp_f32_e32 v125, v125
	v_rcp_f32_e32 v127, v127
	v_rcp_f32_e32 v126, v126
	v_rcp_f32_e32 v128, v128
	v_rcp_f32_e32 v129, v129
	v_mul_f32_e32 v114, v117, v114
	v_mul_f32_e32 v107, v107, v115
	v_mul_f32_e32 v111, v111, v124
	v_mul_f32_e32 v109, v109, v125
	v_mul_f32_e32 v99, v99, v127
	v_mul_f32_e32 v113, v113, v126
	v_mul_f32_e32 v103, v103, v128
	v_mul_f32_e32 v101, v101, v129
	v_mul_f32_e32 v114, v116, v114
	v_mul_f32_e32 v106, v106, v107
	v_mul_f32_e32 v107, v110, v111
	v_mul_f32_e32 v108, v108, v109
	v_mul_f32_e32 v110, v98, v99
	v_cvt_pk_bf16_f32 v98, v114, v106
	v_cvt_pk_bf16_f32 v99, v107, v108
	v_mul_f32_e32 v109, v112, v113
	v_mul_f32_e32 v102, v102, v103
	v_mul_f32_e32 v100, v100, v101
	global_store_dwordx2 v[120:121], v[98:99], off
	v_cvt_pk_bf16_f32 v98, v109, v110
	v_cvt_pk_bf16_f32 v99, v102, v100
	global_store_dwordx2 v[120:121], v[98:99], off offset:128
	s_nop 0
	v_mov_b32_e32 v100, v94
	v_mov_b32_e32 v101, v90
	v_mov_b32_e32 v90, v95
	v_mov_b32_e32 v94, v96
	v_mov_b32_e32 v95, v92
	v_mov_b32_e32 v92, v97
	v_mov_b32_e32 v97, v82
	v_mov_b32_e32 v82, v87
	v_mov_b32_e32 v96, v86
	v_mov_b32_e32 v86, v88
	v_mov_b32_e32 v87, v84
	v_mov_b32_e32 v84, v89
	v_lshlrev_b64 v[102:103], 10, v[104:105]
	v_or_b32_e32 v88, 48, v142
	v_lshl_add_u64 v[102:103], s[12:13], 0, v[102:103]
	v_ashrrev_i32_e32 v89, 31, v88
	v_lshl_add_u64 v[102:103], v[102:103], 0, v[134:135]
	v_lshl_add_u64 v[104:105], v[88:89], 2, s[10:11]
	s_nop 0
	s_waitcnt vmcnt(9)
	v_pk_mul_f32 v[100:101], v[100:101], v[180:181] op_sel_hi:[1,0]
	v_pk_mul_f32 v[90:91], v[90:91], v[180:181] op_sel_hi:[1,0]
	v_pk_mul_f32 v[94:95], v[94:95], v[180:181] op_sel_hi:[1,0]
	v_pk_mul_f32 v[92:93], v[92:93], v[180:181] op_sel_hi:[1,0]
	v_pk_mul_f32 v[82:83], v[82:83], v[180:181] op_sel_hi:[1,0]
	v_pk_mul_f32 v[96:97], v[96:97], v[180:181] op_sel_hi:[1,0]
	v_pk_mul_f32 v[86:87], v[86:87], v[180:181] op_sel_hi:[1,0]
	v_pk_mul_f32 v[84:85], v[84:85], v[180:181] op_sel_hi:[1,0]
	v_mul_f32_e32 v98, 0xbfb8aa3b, v101
	v_mul_f32_e32 v99, 0xbfb8aa3b, v91
	v_mul_f32_e32 v106, 0xbfb8aa3b, v95
	v_mul_f32_e32 v107, 0xbfb8aa3b, v93
	v_mul_f32_e32 v109, 0xbfb8aa3b, v83
	v_mul_f32_e32 v108, 0xbfb8aa3b, v97
	v_mul_f32_e32 v110, 0xbfb8aa3b, v87
	v_mul_f32_e32 v111, 0xbfb8aa3b, v85
	v_exp_f32_e32 v98, v98
	v_exp_f32_e32 v99, v99
	v_exp_f32_e32 v106, v106
	v_exp_f32_e32 v107, v107
	v_exp_f32_e32 v109, v109
	v_exp_f32_e32 v108, v108
	v_exp_f32_e32 v110, v110
	v_exp_f32_e32 v111, v111
	v_add_f32_e32 v98, 1.0, v98
	v_add_f32_e32 v99, 1.0, v99
	v_add_f32_e32 v106, 1.0, v106
	v_add_f32_e32 v107, 1.0, v107
	v_add_f32_e32 v109, 1.0, v109
	v_add_f32_e32 v108, 1.0, v108
	v_add_f32_e32 v110, 1.0, v110
	v_add_f32_e32 v111, 1.0, v111
	v_rcp_f32_e32 v98, v98
	v_rcp_f32_e32 v99, v99
	v_rcp_f32_e32 v106, v106
	v_rcp_f32_e32 v107, v107
	v_rcp_f32_e32 v109, v109
	v_rcp_f32_e32 v108, v108
	v_rcp_f32_e32 v110, v110
	v_rcp_f32_e32 v111, v111
	v_mul_f32_e32 v98, v101, v98
	v_mul_f32_e32 v91, v91, v99
	v_mul_f32_e32 v95, v95, v106
	v_mul_f32_e32 v93, v93, v107
	v_mul_f32_e32 v83, v83, v109
	v_mul_f32_e32 v97, v97, v108
	v_mul_f32_e32 v87, v87, v110
	v_mul_f32_e32 v85, v85, v111
	v_mul_f32_e32 v98, v100, v98
	v_mul_f32_e32 v90, v90, v91
	v_mul_f32_e32 v91, v94, v95
	v_mul_f32_e32 v92, v92, v93
	v_mul_f32_e32 v94, v82, v83
	v_cvt_pk_bf16_f32 v82, v98, v90
	v_cvt_pk_bf16_f32 v83, v91, v92
	v_mul_f32_e32 v93, v96, v97
	v_mul_f32_e32 v86, v86, v87
	v_mul_f32_e32 v84, v84, v85
	global_store_dwordx2 v[102:103], v[82:83], off
	v_cvt_pk_bf16_f32 v82, v93, v94
	v_cvt_pk_bf16_f32 v83, v86, v84
	global_store_dwordx2 v[102:103], v[82:83], off offset:128
	s_nop 0
	v_mov_b32_e32 v84, v78
	v_mov_b32_e32 v85, v74
	v_mov_b32_e32 v74, v79
	v_mov_b32_e32 v78, v80
	v_mov_b32_e32 v79, v76
	v_mov_b32_e32 v76, v81
	v_mov_b32_e32 v81, v66
	v_mov_b32_e32 v66, v71
	v_mov_b32_e32 v80, v70
	v_mov_b32_e32 v70, v72
	v_mov_b32_e32 v71, v68
	v_mov_b32_e32 v68, v73
	v_lshlrev_b64 v[72:73], 10, v[88:89]
	v_lshl_add_u64 v[72:73], s[12:13], 0, v[72:73]
	v_lshl_add_u64 v[72:73], v[72:73], 0, v[134:135]
	s_nop 0
	s_waitcnt vmcnt(10)
; DI float sigmoidf_(float x) { return __builtin_amdgcn_rcpf(1.0f + __expf(-x)); }
; DI unsigned cvt_pk_bf16(float lo, float hi) { unsigned r; asm volatile("v_cvt_pk_bf16_f32 %0, %1, %2" : "=v"(r) : "v"(lo), "v"(hi)); return r; }
;     DI void operator()(const f32x4 (&acc)[2][2][4][2], const pg8::Unit& u, int wr, int wc, int fr, int fq) const {
;         const int row0 = u.pm * 256 + wr * 64 + fr, pnr = u.pn & 3;
; #pragma unroll
;         for (int ai = 0; ai < 2; ++ai)
; #pragma unroll
;             for (int m = 0; m < 4; ++m) {
;                 const int p = row0 + ai * 128 + m * 16; const float r = rowr2[p];
; #pragma unroll
;                 for (int bj = 0; bj < 2; ++bj) {
;                     const int f0 = 128 * pnr + 64 * bj + 16 * wc + 4 * fq;
;                     float o[4];
; #pragma unroll
;                     for (int e = 0; e < 4; ++e) { const float g = acc[ai][bj][m][0][e] * r, up = acc[ai][bj][m][1][e] * r; o[e] = g * sigmoidf_(g) * up; }
;                     u32x2 w; w.x = pg8::cvt_pk_bf16(o[0], o[1]); w.y = pg8::cvt_pk_bf16(o[2], o[3]);
;                     *(u32x2*)(U + (size_t)p * FF + f0) = w;
;                 }
;             }
;     }
	v_pk_mul_f32 v[84:85], v[84:85], v[182:183] op_sel_hi:[1,0]
	v_pk_mul_f32 v[74:75], v[74:75], v[182:183] op_sel_hi:[1,0]
	v_pk_mul_f32 v[78:79], v[78:79], v[182:183] op_sel_hi:[1,0]
	v_pk_mul_f32 v[76:77], v[76:77], v[182:183] op_sel_hi:[1,0]
	v_pk_mul_f32 v[66:67], v[66:67], v[182:183] op_sel_hi:[1,0]
	v_pk_mul_f32 v[80:81], v[80:81], v[182:183] op_sel_hi:[1,0]
	v_pk_mul_f32 v[70:71], v[70:71], v[182:183] op_sel_hi:[1,0]
	v_pk_mul_f32 v[68:69], v[68:69], v[182:183] op_sel_hi:[1,0]
	v_mul_f32_e32 v82, 0xbfb8aa3b, v85
	v_mul_f32_e32 v83, 0xbfb8aa3b, v75
	v_mul_f32_e32 v86, 0xbfb8aa3b, v79
	v_mul_f32_e32 v87, 0xbfb8aa3b, v77
	v_mul_f32_e32 v89, 0xbfb8aa3b, v67
	v_mul_f32_e32 v88, 0xbfb8aa3b, v81
	v_mul_f32_e32 v90, 0xbfb8aa3b, v71
	v_mul_f32_e32 v91, 0xbfb8aa3b, v69
	v_exp_f32_e32 v82, v82
	v_exp_f32_e32 v83, v83
	v_exp_f32_e32 v86, v86
	v_exp_f32_e32 v87, v87
	v_exp_f32_e32 v89, v89
	v_exp_f32_e32 v88, v88
	v_exp_f32_e32 v90, v90
	v_exp_f32_e32 v91, v91
	v_add_f32_e32 v82, 1.0, v82
	v_add_f32_e32 v83, 1.0, v83
	v_add_f32_e32 v86, 1.0, v86
	v_add_f32_e32 v87, 1.0, v87
	v_add_f32_e32 v89, 1.0, v89
	v_add_f32_e32 v88, 1.0, v88
	v_add_f32_e32 v90, 1.0, v90
	v_add_f32_e32 v91, 1.0, v91
	v_rcp_f32_e32 v82, v82
	v_rcp_f32_e32 v83, v83
	v_rcp_f32_e32 v86, v86
	v_rcp_f32_e32 v87, v87
	v_rcp_f32_e32 v89, v89
	v_rcp_f32_e32 v88, v88
	v_rcp_f32_e32 v90, v90
	v_rcp_f32_e32 v91, v91
	v_mul_f32_e32 v82, v85, v82
	v_mul_f32_e32 v75, v75, v83
	v_mul_f32_e32 v79, v79, v86
	v_mul_f32_e32 v77, v77, v87
	v_mul_f32_e32 v67, v67, v89
	v_mul_f32_e32 v81, v81, v88
	v_mul_f32_e32 v71, v71, v90
	v_mul_f32_e32 v69, v69, v91
	v_mul_f32_e32 v82, v84, v82
	v_mul_f32_e32 v74, v74, v75
	v_mul_f32_e32 v75, v78, v79
	v_mul_f32_e32 v76, v76, v77
	v_mul_f32_e32 v78, v66, v67
	v_cvt_pk_bf16_f32 v66, v82, v74
	v_cvt_pk_bf16_f32 v67, v75, v76
	v_mul_f32_e32 v77, v80, v81
	v_mul_f32_e32 v70, v70, v71
	v_mul_f32_e32 v68, v68, v69
	global_store_dwordx2 v[72:73], v[66:67], off
	v_cvt_pk_bf16_f32 v66, v77, v78
	v_cvt_pk_bf16_f32 v67, v70, v68
	global_store_dwordx2 v[72:73], v[66:67], off offset:128
	s_nop 0
	v_mov_b32_e32 v68, v62
	v_mov_b32_e32 v69, v58
	v_mov_b32_e32 v58, v63
	v_mov_b32_e32 v62, v64
	v_mov_b32_e32 v63, v60
	v_mov_b32_e32 v60, v65
	v_mov_b32_e32 v65, v50
	v_mov_b32_e32 v50, v55
	v_mov_b32_e32 v64, v54
	v_mov_b32_e32 v54, v56
	v_mov_b32_e32 v55, v52
	v_mov_b32_e32 v52, v57
	v_add_co_u32_e32 v70, vcc, s49, v118
	v_lshl_add_u64 v[56:57], v[118:119], 0, s[20:21]
	s_nop 0
	v_addc_co_u32_e32 v71, vcc, 0, v119, vcc
	s_nop 0
	s_waitcnt vmcnt(11)
	v_pk_mul_f32 v[68:69], v[68:69], v[184:185] op_sel_hi:[1,0]
	v_pk_mul_f32 v[58:59], v[58:59], v[184:185] op_sel_hi:[1,0]
	v_pk_mul_f32 v[62:63], v[62:63], v[184:185] op_sel_hi:[1,0]
	v_pk_mul_f32 v[60:61], v[60:61], v[184:185] op_sel_hi:[1,0]
	v_pk_mul_f32 v[50:51], v[50:51], v[184:185] op_sel_hi:[1,0]
	v_pk_mul_f32 v[64:65], v[64:65], v[184:185] op_sel_hi:[1,0]
	v_pk_mul_f32 v[54:55], v[54:55], v[184:185] op_sel_hi:[1,0]
	v_pk_mul_f32 v[52:53], v[52:53], v[184:185] op_sel_hi:[1,0]
	v_mul_f32_e32 v66, 0xbfb8aa3b, v69
	v_mul_f32_e32 v67, 0xbfb8aa3b, v59
	v_mul_f32_e32 v72, 0xbfb8aa3b, v63
	v_mul_f32_e32 v73, 0xbfb8aa3b, v61
	v_mul_f32_e32 v75, 0xbfb8aa3b, v51
	v_mul_f32_e32 v74, 0xbfb8aa3b, v65
	v_mul_f32_e32 v76, 0xbfb8aa3b, v55
	v_mul_f32_e32 v77, 0xbfb8aa3b, v53
	v_exp_f32_e32 v66, v66
	v_exp_f32_e32 v67, v67
	v_exp_f32_e32 v72, v72
	v_exp_f32_e32 v73, v73
	v_exp_f32_e32 v75, v75
	v_exp_f32_e32 v74, v74
	v_exp_f32_e32 v76, v76
	v_exp_f32_e32 v77, v77
	v_add_f32_e32 v66, 1.0, v66
	v_add_f32_e32 v67, 1.0, v67
	v_add_f32_e32 v72, 1.0, v72
	v_add_f32_e32 v73, 1.0, v73
	v_add_f32_e32 v75, 1.0, v75
	v_add_f32_e32 v74, 1.0, v74
	v_add_f32_e32 v76, 1.0, v76
	v_add_f32_e32 v77, 1.0, v77
	v_rcp_f32_e32 v66, v66
	v_rcp_f32_e32 v67, v67
	v_rcp_f32_e32 v72, v72
	v_rcp_f32_e32 v73, v73
	v_rcp_f32_e32 v75, v75
	v_rcp_f32_e32 v74, v74
	v_rcp_f32_e32 v76, v76
	v_rcp_f32_e32 v77, v77
	v_mul_f32_e32 v66, v69, v66
	v_mul_f32_e32 v59, v59, v67
	v_mul_f32_e32 v63, v63, v72
	v_mul_f32_e32 v61, v61, v73
	v_mul_f32_e32 v51, v51, v75
	v_mul_f32_e32 v65, v65, v74
	v_mul_f32_e32 v55, v55, v76
	v_mul_f32_e32 v53, v53, v77
	v_mul_f32_e32 v66, v68, v66
	v_mul_f32_e32 v58, v58, v59
	v_mul_f32_e32 v59, v62, v63
	v_mul_f32_e32 v60, v60, v61
	v_mul_f32_e32 v62, v50, v51
	v_cvt_pk_bf16_f32 v50, v66, v58
	v_cvt_pk_bf16_f32 v51, v59, v60
	v_mul_f32_e32 v61, v64, v65
	v_mul_f32_e32 v54, v54, v55
	v_mul_f32_e32 v52, v52, v53
	global_store_dwordx2 v[70:71], v[50:51], off
	v_cvt_pk_bf16_f32 v50, v61, v62
	v_cvt_pk_bf16_f32 v51, v54, v52
	global_store_dwordx2 v[56:57], v[50:51], off offset:128
	s_nop 0
	v_mov_b32_e32 v52, v46
	v_mov_b32_e32 v53, v42
	v_mov_b32_e32 v42, v47
	v_mov_b32_e32 v46, v48
	v_mov_b32_e32 v47, v44
	v_mov_b32_e32 v44, v49
	v_mov_b32_e32 v49, v34
	v_mov_b32_e32 v34, v39
	v_mov_b32_e32 v48, v38
	v_mov_b32_e32 v38, v40
	v_mov_b32_e32 v39, v36
	v_mov_b32_e32 v36, v41
	v_add_co_u32_e32 v54, vcc, s55, v118
	v_lshl_add_u64 v[40:41], v[118:119], 0, s[22:23]
	s_nop 0
	v_addc_co_u32_e32 v55, vcc, 0, v119, vcc
	s_nop 0
	s_waitcnt vmcnt(12)
; DI float sigmoidf_(float x) { return __builtin_amdgcn_rcpf(1.0f + __expf(-x)); }
; DI unsigned cvt_pk_bf16(float lo, float hi) { unsigned r; asm volatile("v_cvt_pk_bf16_f32 %0, %1, %2" : "=v"(r) : "v"(lo), "v"(hi)); return r; }
;     DI void operator()(const f32x4 (&acc)[2][2][4][2], const pg8::Unit& u, int wr, int wc, int fr, int fq) const {
;         const int row0 = u.pm * 256 + wr * 64 + fr, pnr = u.pn & 3;
; #pragma unroll
;         for (int ai = 0; ai < 2; ++ai)
; #pragma unroll
;             for (int m = 0; m < 4; ++m) {
;                 const int p = row0 + ai * 128 + m * 16; const float r = rowr2[p];
; #pragma unroll
;                 for (int bj = 0; bj < 2; ++bj) {
;                     const int f0 = 128 * pnr + 64 * bj + 16 * wc + 4 * fq;
;                     float o[4];
; #pragma unroll
;                     for (int e = 0; e < 4; ++e) { const float g = acc[ai][bj][m][0][e] * r, up = acc[ai][bj][m][1][e] * r; o[e] = g * sigmoidf_(g) * up; }
;                     u32x2 w; w.x = pg8::cvt_pk_bf16(o[0], o[1]); w.y = pg8::cvt_pk_bf16(o[2], o[3]);
;                     *(u32x2*)(U + (size_t)p * FF + f0) = w;
;                 }
;             }
;     }
	v_pk_mul_f32 v[52:53], v[52:53], v[186:187] op_sel_hi:[1,0]
	v_pk_mul_f32 v[42:43], v[42:43], v[186:187] op_sel_hi:[1,0]
	v_pk_mul_f32 v[46:47], v[46:47], v[186:187] op_sel_hi:[1,0]
	v_pk_mul_f32 v[44:45], v[44:45], v[186:187] op_sel_hi:[1,0]
	v_pk_mul_f32 v[34:35], v[34:35], v[186:187] op_sel_hi:[1,0]
	v_pk_mul_f32 v[48:49], v[48:49], v[186:187] op_sel_hi:[1,0]
	v_pk_mul_f32 v[38:39], v[38:39], v[186:187] op_sel_hi:[1,0]
	v_pk_mul_f32 v[36:37], v[36:37], v[186:187] op_sel_hi:[1,0]
	v_mul_f32_e32 v50, 0xbfb8aa3b, v53
	v_mul_f32_e32 v51, 0xbfb8aa3b, v43
	v_mul_f32_e32 v56, 0xbfb8aa3b, v47
	v_mul_f32_e32 v57, 0xbfb8aa3b, v45
	v_mul_f32_e32 v59, 0xbfb8aa3b, v35
	v_mul_f32_e32 v58, 0xbfb8aa3b, v49
	v_mul_f32_e32 v60, 0xbfb8aa3b, v39
	v_mul_f32_e32 v61, 0xbfb8aa3b, v37
	v_exp_f32_e32 v50, v50
	v_exp_f32_e32 v51, v51
	v_exp_f32_e32 v56, v56
	v_exp_f32_e32 v57, v57
	v_exp_f32_e32 v59, v59
	v_exp_f32_e32 v58, v58
	v_exp_f32_e32 v60, v60
	v_exp_f32_e32 v61, v61
	v_add_f32_e32 v50, 1.0, v50
	v_add_f32_e32 v51, 1.0, v51
	v_add_f32_e32 v56, 1.0, v56
	v_add_f32_e32 v57, 1.0, v57
	v_add_f32_e32 v59, 1.0, v59
	v_add_f32_e32 v58, 1.0, v58
	v_add_f32_e32 v60, 1.0, v60
	v_add_f32_e32 v61, 1.0, v61
	v_rcp_f32_e32 v50, v50
	v_rcp_f32_e32 v51, v51
	v_rcp_f32_e32 v56, v56
	v_rcp_f32_e32 v57, v57
	v_rcp_f32_e32 v59, v59
	v_rcp_f32_e32 v58, v58
	v_rcp_f32_e32 v60, v60
	v_rcp_f32_e32 v61, v61
	v_mul_f32_e32 v50, v53, v50
	v_mul_f32_e32 v43, v43, v51
	v_mul_f32_e32 v47, v47, v56
	v_mul_f32_e32 v45, v45, v57
	v_mul_f32_e32 v35, v35, v59
	v_mul_f32_e32 v49, v49, v58
	v_mul_f32_e32 v39, v39, v60
	v_mul_f32_e32 v37, v37, v61
	v_mul_f32_e32 v50, v52, v50
	v_mul_f32_e32 v42, v42, v43
	v_mul_f32_e32 v43, v46, v47
	v_mul_f32_e32 v44, v44, v45
	v_mul_f32_e32 v46, v34, v35
	v_cvt_pk_bf16_f32 v34, v50, v42
	v_cvt_pk_bf16_f32 v35, v43, v44
	v_mul_f32_e32 v45, v48, v49
	v_mul_f32_e32 v38, v38, v39
	v_mul_f32_e32 v36, v36, v37
	global_store_dwordx2 v[54:55], v[34:35], off
	v_cvt_pk_bf16_f32 v34, v45, v46
	v_cvt_pk_bf16_f32 v35, v38, v36
	global_store_dwordx2 v[40:41], v[34:35], off offset:128
	s_nop 0
	v_mov_b32_e32 v36, v30
	v_mov_b32_e32 v37, v26
	v_mov_b32_e32 v26, v31
	v_mov_b32_e32 v30, v32
	v_mov_b32_e32 v31, v28
	v_mov_b32_e32 v28, v33
	v_mov_b32_e32 v33, v18
	v_mov_b32_e32 v18, v23
	v_mov_b32_e32 v32, v22
	v_mov_b32_e32 v22, v24
	v_mov_b32_e32 v23, v20
	v_mov_b32_e32 v20, v25
	v_add_co_u32_e32 v38, vcc, s56, v118
	v_lshl_add_u64 v[24:25], v[118:119], 0, s[24:25]
	s_nop 0
	v_addc_co_u32_e32 v39, vcc, 0, v119, vcc
	s_and_b64 vcc, exec, s[2:3]
	s_nop 0
	s_waitcnt vmcnt(13)
; DI float sigmoidf_(float x) { return __builtin_amdgcn_rcpf(1.0f + __expf(-x)); }
; DI unsigned cvt_pk_bf16(float lo, float hi) { unsigned r; asm volatile("v_cvt_pk_bf16_f32 %0, %1, %2" : "=v"(r) : "v"(lo), "v"(hi)); return r; }
; #define PG8_BAR __builtin_amdgcn_s_barrier()
; template <class Epi, class Sched, bool ALIGN_EPI, bool SP2, bool GATHER>
; DI void gemm_phase(LAS unsigned char* lds, const Gemm g, const Sched& S, const Epi& E) {
;     ...
;         E(acc, cur, wr, wc, fr, fq);
;         if (!has_next) break;
; #pragma unroll
;         for (int a = 0; a < 2; ++a)
; #pragma unroll
;             for (int b = 0; b < 2; ++b)
; #pragma unroll
;                 for (int m = 0; m < 4; ++m)
; #pragma unroll
;                     for (int n = 0; n < 2; ++n) acc[a][b][m][n] = (f32x4){0.f, 0.f, 0.f, 0.f};
;         cur = nxt; cA = nA; cB = nB; ++ui;
; #pragma unroll
;         for (int h = 0; h < 2; ++h) { gC[h][0] = gN[h][0]; gC[h][1] = gN[h][1]; }
;         if constexpr (ALIGN_EPI) { if (wr == 1) PG8_BAR; }
;     }
;     DI void operator()(const f32x4 (&acc)[2][2][4][2], const pg8::Unit& u, int wr, int wc, int fr, int fq) const {
;         const int row0 = u.pm * 256 + wr * 64 + fr, pnr = u.pn & 3;
; #pragma unroll
;         for (int ai = 0; ai < 2; ++ai)
; #pragma unroll
;             for (int m = 0; m < 4; ++m) {
;                 const int p = row0 + ai * 128 + m * 16; const float r = rowr2[p];
; #pragma unroll
;                 for (int bj = 0; bj < 2; ++bj) {
;                     const int f0 = 128 * pnr + 64 * bj + 16 * wc + 4 * fq;
;                     float o[4];
; #pragma unroll
;                     for (int e = 0; e < 4; ++e) { const float g = acc[ai][bj][m][0][e] * r, up = acc[ai][bj][m][1][e] * r; o[e] = g * sigmoidf_(g) * up; }
;                     u32x2 w; w.x = pg8::cvt_pk_bf16(o[0], o[1]); w.y = pg8::cvt_pk_bf16(o[2], o[3]);
;                     *(u32x2*)(U + (size_t)p * FF + f0) = w;
;                 }
;             }
;     }
	v_pk_mul_f32 v[36:37], v[36:37], v[188:189] op_sel_hi:[1,0]
	v_pk_mul_f32 v[26:27], v[26:27], v[188:189] op_sel_hi:[1,0]
	v_pk_mul_f32 v[30:31], v[30:31], v[188:189] op_sel_hi:[1,0]
	v_pk_mul_f32 v[28:29], v[28:29], v[188:189] op_sel_hi:[1,0]
	v_pk_mul_f32 v[18:19], v[18:19], v[188:189] op_sel_hi:[1,0]
	v_pk_mul_f32 v[32:33], v[32:33], v[188:189] op_sel_hi:[1,0]
	v_pk_mul_f32 v[22:23], v[22:23], v[188:189] op_sel_hi:[1,0]
	v_pk_mul_f32 v[20:21], v[20:21], v[188:189] op_sel_hi:[1,0]
	v_mul_f32_e32 v34, 0xbfb8aa3b, v37
	v_mul_f32_e32 v35, 0xbfb8aa3b, v27
	v_mul_f32_e32 v40, 0xbfb8aa3b, v31
	v_mul_f32_e32 v41, 0xbfb8aa3b, v29
	v_mul_f32_e32 v43, 0xbfb8aa3b, v19
	v_mul_f32_e32 v42, 0xbfb8aa3b, v33
	v_mul_f32_e32 v44, 0xbfb8aa3b, v23
	v_mul_f32_e32 v45, 0xbfb8aa3b, v21
	v_exp_f32_e32 v34, v34
	v_exp_f32_e32 v35, v35
	v_exp_f32_e32 v40, v40
	v_exp_f32_e32 v41, v41
	v_exp_f32_e32 v43, v43
	v_exp_f32_e32 v42, v42
	v_exp_f32_e32 v44, v44
	v_exp_f32_e32 v45, v45
	v_add_f32_e32 v34, 1.0, v34
	v_add_f32_e32 v35, 1.0, v35
	v_add_f32_e32 v40, 1.0, v40
	v_add_f32_e32 v41, 1.0, v41
	v_add_f32_e32 v43, 1.0, v43
	v_add_f32_e32 v42, 1.0, v42
	v_add_f32_e32 v44, 1.0, v44
	v_add_f32_e32 v45, 1.0, v45
	v_rcp_f32_e32 v34, v34
	v_rcp_f32_e32 v35, v35
	v_rcp_f32_e32 v40, v40
	v_rcp_f32_e32 v41, v41
	v_rcp_f32_e32 v43, v43
	v_rcp_f32_e32 v42, v42
	v_rcp_f32_e32 v44, v44
	v_rcp_f32_e32 v45, v45
	v_mul_f32_e32 v34, v37, v34
	v_mul_f32_e32 v27, v27, v35
	v_mul_f32_e32 v31, v31, v40
	v_mul_f32_e32 v29, v29, v41
	v_mul_f32_e32 v19, v19, v43
	v_mul_f32_e32 v33, v33, v42
	v_mul_f32_e32 v23, v23, v44
	v_mul_f32_e32 v21, v21, v45
	v_mul_f32_e32 v34, v36, v34
	v_mul_f32_e32 v26, v26, v27
	v_mul_f32_e32 v27, v30, v31
	v_mul_f32_e32 v28, v28, v29
	v_mul_f32_e32 v30, v18, v19
	v_cvt_pk_bf16_f32 v18, v34, v26
	v_cvt_pk_bf16_f32 v19, v27, v28
	v_mul_f32_e32 v29, v32, v33
	v_mul_f32_e32 v22, v22, v23
	v_mul_f32_e32 v20, v20, v21
	global_store_dwordx2 v[38:39], v[18:19], off
	v_cvt_pk_bf16_f32 v18, v29, v30
	v_cvt_pk_bf16_f32 v19, v22, v20
	global_store_dwordx2 v[24:25], v[18:19], off offset:128
	s_nop 0
	v_mov_b32_e32 v20, v14
	v_mov_b32_e32 v21, v10
	v_mov_b32_e32 v10, v15
	v_mov_b32_e32 v14, v16
	v_mov_b32_e32 v15, v12
	v_mov_b32_e32 v12, v17
	v_mov_b32_e32 v17, v2
	v_mov_b32_e32 v2, v7
	v_mov_b32_e32 v16, v6
	v_mov_b32_e32 v6, v8
	v_mov_b32_e32 v7, v4
	v_mov_b32_e32 v4, v9
	v_add_co_u32_e64 v22, s[2:3], s57, v118
	v_lshl_add_u64 v[8:9], v[118:119], 0, s[26:27]
	s_nop 0
	v_addc_co_u32_e64 v23, s[2:3], 0, v119, s[2:3]
	s_mov_b64 s[2:3], -1
	s_nop 0
	s_waitcnt vmcnt(14)
	v_pk_mul_f32 v[20:21], v[20:21], v[190:191] op_sel_hi:[1,0]
	v_pk_mul_f32 v[10:11], v[10:11], v[190:191] op_sel_hi:[1,0]
	v_pk_mul_f32 v[14:15], v[14:15], v[190:191] op_sel_hi:[1,0]
	v_pk_mul_f32 v[12:13], v[12:13], v[190:191] op_sel_hi:[1,0]
	v_pk_mul_f32 v[2:3], v[2:3], v[190:191] op_sel_hi:[1,0]
	v_pk_mul_f32 v[16:17], v[16:17], v[190:191] op_sel_hi:[1,0]
	v_pk_mul_f32 v[6:7], v[6:7], v[190:191] op_sel_hi:[1,0]
	v_pk_mul_f32 v[4:5], v[4:5], v[190:191] op_sel_hi:[1,0]
	v_mul_f32_e32 v18, 0xbfb8aa3b, v21
	v_mul_f32_e32 v19, 0xbfb8aa3b, v11
	v_mul_f32_e32 v24, 0xbfb8aa3b, v15
	v_mul_f32_e32 v25, 0xbfb8aa3b, v13
	v_mul_f32_e32 v27, 0xbfb8aa3b, v3
	v_mul_f32_e32 v26, 0xbfb8aa3b, v17
	v_mul_f32_e32 v28, 0xbfb8aa3b, v7
	v_mul_f32_e32 v29, 0xbfb8aa3b, v5
	v_exp_f32_e32 v18, v18
	v_exp_f32_e32 v19, v19
	v_exp_f32_e32 v24, v24
	v_exp_f32_e32 v25, v25
	v_exp_f32_e32 v27, v27
	v_exp_f32_e32 v26, v26
	v_exp_f32_e32 v28, v28
	v_exp_f32_e32 v29, v29
	v_add_f32_e32 v18, 1.0, v18
	v_add_f32_e32 v19, 1.0, v19
	v_add_f32_e32 v24, 1.0, v24
	v_add_f32_e32 v25, 1.0, v25
	v_add_f32_e32 v27, 1.0, v27
	v_add_f32_e32 v26, 1.0, v26
	v_add_f32_e32 v28, 1.0, v28
	v_add_f32_e32 v29, 1.0, v29
	v_rcp_f32_e32 v18, v18
	v_rcp_f32_e32 v19, v19
	v_rcp_f32_e32 v24, v24
	v_rcp_f32_e32 v25, v25
	v_rcp_f32_e32 v27, v27
	v_rcp_f32_e32 v26, v26
	v_rcp_f32_e32 v28, v28
	v_rcp_f32_e32 v29, v29
	v_mul_f32_e32 v18, v21, v18
	v_mul_f32_e32 v11, v11, v19
	v_mul_f32_e32 v15, v15, v24
	v_mul_f32_e32 v13, v13, v25
	v_mul_f32_e32 v3, v3, v27
	v_mul_f32_e32 v17, v17, v26
	v_mul_f32_e32 v7, v7, v28
	v_mul_f32_e32 v5, v5, v29
	v_mul_f32_e32 v18, v20, v18
	v_mul_f32_e32 v10, v10, v11
	v_mul_f32_e32 v11, v14, v15
	v_mul_f32_e32 v12, v12, v13
	v_mul_f32_e32 v14, v2, v3
	v_cvt_pk_bf16_f32 v2, v18, v10
	v_cvt_pk_bf16_f32 v3, v11, v12
	v_mul_f32_e32 v13, v16, v17
	v_mul_f32_e32 v6, v6, v7
	v_mul_f32_e32 v4, v4, v5
	global_store_dwordx2 v[22:23], v[2:3], off
	v_cvt_pk_bf16_f32 v2, v13, v14
	v_cvt_pk_bf16_f32 v3, v6, v4
	global_store_dwordx2 v[8:9], v[2:3], off offset:128
	s_cbranch_vccnz .LBB0_899
	s_andn2_b64 vcc, exec, s[8:9]
	s_cbranch_vccnz .LBB0_898
	s_barrier
	s_branch .LBB0_898

; DI unsigned cvt_pk_bf16(float lo, float hi) { unsigned r; asm volatile("v_cvt_pk_bf16_f32 %0, %1, %2" : "=v"(r) : "v"(lo), "v"(hi)); return r; }
;     DI void operator()(const f32x4 (&acc)[2][2][4][2], const pg8::Unit& u, int wr, int wc, int fr, int fq) const {
;         const int row0 = u.pm * 256 + wr * 64 + fr, col0 = (u.pn & 7) * 256 + wc * 32 + 8 * fq;
; #pragma unroll
;         for (int ai = 0; ai < 2; ++ai)
; #pragma unroll
;             for (int m = 0; m < 4; ++m) {
;                 const int p = row0 + ai * 128 + m * 16; const int dst = rowdst[p]; const float w = roww[p];
;                 if (dst >= 0) {
; #pragma unroll
;                     for (int bj = 0; bj < 2; ++bj) {
;                         const f32x4 a0 = acc[ai][bj][m][0] * w, a1 = acc[ai][bj][m][1] * w;
;                         u32x4 o; o.x = pg8::cvt_pk_bf16(a0[0], a0[1]); o.y = pg8::cvt_pk_bf16(a0[2], a0[3]); o.z = pg8::cvt_pk_bf16(a1[0], a1[1]); o.w = pg8::cvt_pk_bf16(a1[2], a1[3]);
;                         *(u32x4*)(YK + (size_t)dst * D + col0 + bj * 128) = o;
;                     }
;                 }
;             }
;     }
.LBB0_999:
	v_lshl_add_u32 v164, s26, 8, v1
	v_ashrrev_i32_e32 v165, 31, v164
	v_lshl_add_u64 v[166:167], v[164:165], 2, s[4:5]
	global_load_dword v176, v[166:167], off
	v_mov_b32_e32 v177, v139
	v_lshl_add_u64 v[168:169], v[164:165], 2, s[6:7]
	global_load_dword v178, v[168:169], off
	v_or_b32_e32 v170, 16, v164
	v_ashrrev_i32_e32 v171, 31, v170
	v_lshl_add_u64 v[172:173], v[170:171], 2, s[4:5]
	global_load_dword v180, v[172:173], off
	v_mov_b32_e32 v181, v139
	v_lshl_add_u64 v[172:173], v[170:171], 2, s[6:7]
	global_load_dword v182, v[172:173], off
	v_or_b32_e32 v170, 32, v164
	v_ashrrev_i32_e32 v171, 31, v170
	v_lshl_add_u64 v[172:173], v[170:171], 2, s[4:5]
	global_load_dword v184, v[172:173], off
	v_mov_b32_e32 v185, v139
	v_lshl_add_u64 v[172:173], v[170:171], 2, s[6:7]
	global_load_dword v186, v[172:173], off
	v_or_b32_e32 v170, 48, v164
	v_ashrrev_i32_e32 v171, 31, v170
	v_lshl_add_u64 v[164:165], v[170:171], 2, s[4:5]
	global_load_dword v188, v[164:165], off
	v_mov_b32_e32 v189, v139
	v_lshl_add_u64 v[164:165], v[170:171], 2, s[6:7]
	global_load_dword v190, v[164:165], off
	global_load_dword v192, v[166:167], off offset:512
	v_mov_b32_e32 v193, v139
	global_load_dword v194, v[168:169], off offset:512
	global_load_dword v196, v[166:167], off offset:576
	v_mov_b32_e32 v197, v139
	global_load_dword v198, v[168:169], off offset:576
	global_load_dword v200, v[166:167], off offset:640
	v_mov_b32_e32 v201, v139
	global_load_dword v202, v[168:169], off offset:640
	global_load_dword v204, v[166:167], off offset:704
	v_mov_b32_e32 v205, v139
	global_load_dword v206, v[168:169], off offset:704
	s_waitcnt vmcnt(0)
	v_lshl_add_u32 v150, s26, 8, v1
	v_ashrrev_i32_e32 v151, 31, v150
	v_lshl_add_u64 v[148:149], v[150:151], 2, s[4:5]
	s_nop 0
	s_lshl_b32 s15, s24, 8
	s_and_b32 s15, s15, 0x700
	v_or_b32_e32 v144, s15, v153
	v_lshl_add_u64 v[146:147], v[150:151], 2, s[6:7]
	v_lshlrev_b32_e32 v144, 1, v144
	s_nop 0
	v_cmp_lt_i32_e32 vcc, -1, v176
	s_and_saveexec_b64 s[24:25], vcc
	s_nop 0
	v_lshlrev_b64 v[160:161], 12, v[176:177]
	v_mov_b32_e32 v145, v139
	v_lshl_add_u64 v[160:161], s[8:9], 0, v[160:161]
	v_lshl_add_u64 v[160:161], v[160:161], 0, v[144:145]
	s_nop 0
	v_pk_mul_f32 v[128:129], v[128:129], v[178:179] op_sel_hi:[1,0]
	v_pk_mul_f32 v[126:127], v[126:127], v[178:179] op_sel_hi:[1,0]
	v_pk_mul_f32 v[124:125], v[124:125], v[178:179] op_sel_hi:[1,0]
	v_pk_mul_f32 v[122:123], v[122:123], v[178:179] op_sel_hi:[1,0]
	v_pk_mul_f32 v[120:121], v[120:121], v[178:179] op_sel_hi:[1,0]
	v_pk_mul_f32 v[118:119], v[118:119], v[178:179] op_sel_hi:[1,0]
	v_pk_mul_f32 v[162:163], v[116:117], v[178:179] op_sel_hi:[1,0]
	v_pk_mul_f32 v[158:159], v[114:115], v[178:179] op_sel_hi:[1,0]
	v_cvt_pk_bf16_f32 v114, v126, v127
	v_cvt_pk_bf16_f32 v115, v128, v129
	v_cvt_pk_bf16_f32 v116, v122, v123
	v_cvt_pk_bf16_f32 v117, v124, v125
	global_store_dwordx4 v[160:161], v[114:117], off
	s_nop 1
	v_cvt_pk_bf16_f32 v114, v118, v119
	v_cvt_pk_bf16_f32 v115, v120, v121
	v_cvt_pk_bf16_f32 v116, v158, v159
	v_cvt_pk_bf16_f32 v117, v162, v163
	global_store_dwordx4 v[160:161], v[114:117], off offset:256
	s_or_b64 exec, exec, s[24:25]
	s_nop 0
	v_or_b32_e32 v114, 16, v150
	v_ashrrev_i32_e32 v115, 31, v114
	v_lshl_add_u64 v[116:117], v[114:115], 2, s[4:5]
	s_nop 0
	s_nop 0
	v_cmp_lt_i32_e32 vcc, -1, v180
	s_and_saveexec_b64 s[24:25], vcc
	v_lshl_add_u64 v[114:115], v[114:115], 2, s[6:7]
	s_nop 0
	v_lshlrev_b64 v[116:117], 12, v[180:181]
	v_mov_b32_e32 v145, v139
	v_lshl_add_u64 v[116:117], s[8:9], 0, v[116:117]
	v_lshl_add_u64 v[116:117], v[116:117], 0, v[144:145]
	s_nop 0
	v_pk_mul_f32 v[112:113], v[112:113], v[182:183] op_sel_hi:[1,0]
	v_pk_mul_f32 v[110:111], v[110:111], v[182:183] op_sel_hi:[1,0]
	v_pk_mul_f32 v[108:109], v[108:109], v[182:183] op_sel_hi:[1,0]
	v_pk_mul_f32 v[106:107], v[106:107], v[182:183] op_sel_hi:[1,0]
	v_pk_mul_f32 v[104:105], v[104:105], v[182:183] op_sel_hi:[1,0]
	v_pk_mul_f32 v[102:103], v[102:103], v[182:183] op_sel_hi:[1,0]
	v_pk_mul_f32 v[118:119], v[100:101], v[182:183] op_sel_hi:[1,0]
	v_pk_mul_f32 v[114:115], v[98:99], v[182:183] op_sel_hi:[1,0]
	v_cvt_pk_bf16_f32 v98, v110, v111
	v_cvt_pk_bf16_f32 v99, v112, v113
	v_cvt_pk_bf16_f32 v100, v106, v107
	v_cvt_pk_bf16_f32 v101, v108, v109
	global_store_dwordx4 v[116:117], v[98:101], off
	s_nop 1
	v_cvt_pk_bf16_f32 v98, v102, v103
	v_cvt_pk_bf16_f32 v99, v104, v105
	v_cvt_pk_bf16_f32 v100, v114, v115
	v_cvt_pk_bf16_f32 v101, v118, v119
	global_store_dwordx4 v[116:117], v[98:101], off offset:256
	s_or_b64 exec, exec, s[24:25]
	s_nop 0
	v_or_b32_e32 v98, 32, v150
	v_ashrrev_i32_e32 v99, 31, v98
	v_lshl_add_u64 v[100:101], v[98:99], 2, s[4:5]
	s_nop 0
	s_nop 0
	v_cmp_lt_i32_e32 vcc, -1, v184
	s_and_saveexec_b64 s[24:25], vcc
	v_lshl_add_u64 v[98:99], v[98:99], 2, s[6:7]
	s_nop 0
	v_lshlrev_b64 v[100:101], 12, v[184:185]
	v_mov_b32_e32 v145, v139
	v_lshl_add_u64 v[100:101], s[8:9], 0, v[100:101]
	v_lshl_add_u64 v[100:101], v[100:101], 0, v[144:145]
	s_nop 0
	v_pk_mul_f32 v[96:97], v[96:97], v[186:187] op_sel_hi:[1,0]
	v_pk_mul_f32 v[94:95], v[94:95], v[186:187] op_sel_hi:[1,0]
	v_pk_mul_f32 v[92:93], v[92:93], v[186:187] op_sel_hi:[1,0]
	v_pk_mul_f32 v[90:91], v[90:91], v[186:187] op_sel_hi:[1,0]
	v_pk_mul_f32 v[88:89], v[88:89], v[186:187] op_sel_hi:[1,0]
	v_pk_mul_f32 v[86:87], v[86:87], v[186:187] op_sel_hi:[1,0]
	v_pk_mul_f32 v[102:103], v[84:85], v[186:187] op_sel_hi:[1,0]
	v_pk_mul_f32 v[98:99], v[82:83], v[186:187] op_sel_hi:[1,0]
	v_cvt_pk_bf16_f32 v82, v94, v95
	v_cvt_pk_bf16_f32 v83, v96, v97
	v_cvt_pk_bf16_f32 v84, v90, v91
	v_cvt_pk_bf16_f32 v85, v92, v93
	global_store_dwordx4 v[100:101], v[82:85], off
; DI unsigned cvt_pk_bf16(float lo, float hi) { unsigned r; asm volatile("v_cvt_pk_bf16_f32 %0, %1, %2" : "=v"(r) : "v"(lo), "v"(hi)); return r; }
; #define PG8_BAR __builtin_amdgcn_s_barrier()
; template <class Epi, class Sched, bool ALIGN_EPI, bool SP2, bool GATHER>
; DI void gemm_phase(LAS unsigned char* lds, const Gemm g, const Sched& S, const Epi& E) {
;     ...
;         E(acc, cur, wr, wc, fr, fq);
;         if (!has_next) break;
; #pragma unroll
;         for (int a = 0; a < 2; ++a)
; #pragma unroll
;             for (int b = 0; b < 2; ++b)
; #pragma unroll
;                 for (int m = 0; m < 4; ++m)
; #pragma unroll
;                     for (int n = 0; n < 2; ++n) acc[a][b][m][n] = (f32x4){0.f, 0.f, 0.f, 0.f};
;         cur = nxt; cA = nA; cB = nB; ++ui;
; #pragma unroll
;         for (int h = 0; h < 2; ++h) { gC[h][0] = gN[h][0]; gC[h][1] = gN[h][1]; }
;         if constexpr (ALIGN_EPI) { if (wr == 1) PG8_BAR; }
;     }
;     DI void operator()(const f32x4 (&acc)[2][2][4][2], const pg8::Unit& u, int wr, int wc, int fr, int fq) const {
;         const int row0 = u.pm * 256 + wr * 64 + fr, col0 = (u.pn & 7) * 256 + wc * 32 + 8 * fq;
; #pragma unroll
;         for (int ai = 0; ai < 2; ++ai)
; #pragma unroll
;             for (int m = 0; m < 4; ++m) {
;                 const int p = row0 + ai * 128 + m * 16; const int dst = rowdst[p]; const float w = roww[p];
;                 if (dst >= 0) {
; #pragma unroll
;                     for (int bj = 0; bj < 2; ++bj) {
;                         const f32x4 a0 = acc[ai][bj][m][0] * w, a1 = acc[ai][bj][m][1] * w;
;                         u32x4 o; o.x = pg8::cvt_pk_bf16(a0[0], a0[1]); o.y = pg8::cvt_pk_bf16(a0[2], a0[3]); o.z = pg8::cvt_pk_bf16(a1[0], a1[1]); o.w = pg8::cvt_pk_bf16(a1[2], a1[3]);
;                         *(u32x4*)(YK + (size_t)dst * D + col0 + bj * 128) = o;
;                     }
;                 }
;             }
;     }
	s_nop 1
	v_cvt_pk_bf16_f32 v82, v86, v87
	v_cvt_pk_bf16_f32 v83, v88, v89
	v_cvt_pk_bf16_f32 v84, v98, v99
	v_cvt_pk_bf16_f32 v85, v102, v103
	global_store_dwordx4 v[100:101], v[82:85], off offset:256
	s_or_b64 exec, exec, s[24:25]
	s_nop 0
	v_or_b32_e32 v82, 48, v150
	v_ashrrev_i32_e32 v83, 31, v82
	v_lshl_add_u64 v[84:85], v[82:83], 2, s[4:5]
	s_nop 0
	s_nop 0
	v_cmp_lt_i32_e32 vcc, -1, v188
	s_and_saveexec_b64 s[24:25], vcc
	v_lshl_add_u64 v[82:83], v[82:83], 2, s[6:7]
	s_nop 0
	v_lshlrev_b64 v[84:85], 12, v[188:189]
	v_mov_b32_e32 v145, v139
	v_lshl_add_u64 v[84:85], s[8:9], 0, v[84:85]
	v_lshl_add_u64 v[84:85], v[84:85], 0, v[144:145]
	s_nop 0
	v_pk_mul_f32 v[80:81], v[80:81], v[190:191] op_sel_hi:[1,0]
	v_pk_mul_f32 v[78:79], v[78:79], v[190:191] op_sel_hi:[1,0]
	v_pk_mul_f32 v[76:77], v[76:77], v[190:191] op_sel_hi:[1,0]
	v_pk_mul_f32 v[74:75], v[74:75], v[190:191] op_sel_hi:[1,0]
	v_pk_mul_f32 v[72:73], v[72:73], v[190:191] op_sel_hi:[1,0]
	v_pk_mul_f32 v[70:71], v[70:71], v[190:191] op_sel_hi:[1,0]
	v_pk_mul_f32 v[86:87], v[68:69], v[190:191] op_sel_hi:[1,0]
	v_pk_mul_f32 v[82:83], v[66:67], v[190:191] op_sel_hi:[1,0]
	v_cvt_pk_bf16_f32 v66, v78, v79
	v_cvt_pk_bf16_f32 v67, v80, v81
	v_cvt_pk_bf16_f32 v68, v74, v75
	v_cvt_pk_bf16_f32 v69, v76, v77
	global_store_dwordx4 v[84:85], v[66:69], off
	s_nop 1
	v_cvt_pk_bf16_f32 v66, v70, v71
	v_cvt_pk_bf16_f32 v67, v72, v73
	v_cvt_pk_bf16_f32 v68, v82, v83
	v_cvt_pk_bf16_f32 v69, v86, v87
	global_store_dwordx4 v[84:85], v[66:69], off offset:256
	s_or_b64 exec, exec, s[24:25]
	s_nop 0
	s_nop 0
	v_cmp_lt_i32_e32 vcc, -1, v192
	s_and_saveexec_b64 s[24:25], vcc
	s_nop 0
	v_lshlrev_b64 v[68:69], 12, v[192:193]
	v_mov_b32_e32 v145, v139
	v_lshl_add_u64 v[68:69], s[8:9], 0, v[68:69]
	v_lshl_add_u64 v[68:69], v[68:69], 0, v[144:145]
	s_nop 0
	v_pk_mul_f32 v[64:65], v[64:65], v[194:195] op_sel_hi:[1,0]
	v_pk_mul_f32 v[62:63], v[62:63], v[194:195] op_sel_hi:[1,0]
	v_pk_mul_f32 v[60:61], v[60:61], v[194:195] op_sel_hi:[1,0]
	v_pk_mul_f32 v[58:59], v[58:59], v[194:195] op_sel_hi:[1,0]
	v_pk_mul_f32 v[56:57], v[56:57], v[194:195] op_sel_hi:[1,0]
	v_pk_mul_f32 v[54:55], v[54:55], v[194:195] op_sel_hi:[1,0]
	v_pk_mul_f32 v[70:71], v[52:53], v[194:195] op_sel_hi:[1,0]
	v_pk_mul_f32 v[66:67], v[50:51], v[194:195] op_sel_hi:[1,0]
	v_cvt_pk_bf16_f32 v50, v62, v63
	v_cvt_pk_bf16_f32 v51, v64, v65
	v_cvt_pk_bf16_f32 v52, v58, v59
	v_cvt_pk_bf16_f32 v53, v60, v61
	global_store_dwordx4 v[68:69], v[50:53], off
	s_nop 1
	v_cvt_pk_bf16_f32 v50, v54, v55
	v_cvt_pk_bf16_f32 v51, v56, v57
	v_cvt_pk_bf16_f32 v52, v66, v67
	v_cvt_pk_bf16_f32 v53, v70, v71
	global_store_dwordx4 v[68:69], v[50:53], off offset:256
	s_or_b64 exec, exec, s[24:25]
	s_nop 0
	s_nop 0
	v_cmp_lt_i32_e32 vcc, -1, v196
	s_and_saveexec_b64 s[24:25], vcc
	s_nop 0
	v_lshlrev_b64 v[52:53], 12, v[196:197]
	v_mov_b32_e32 v145, v139
	v_lshl_add_u64 v[52:53], s[8:9], 0, v[52:53]
	v_lshl_add_u64 v[52:53], v[52:53], 0, v[144:145]
	s_nop 0
	v_pk_mul_f32 v[48:49], v[48:49], v[198:199] op_sel_hi:[1,0]
	v_pk_mul_f32 v[46:47], v[46:47], v[198:199] op_sel_hi:[1,0]
	v_pk_mul_f32 v[44:45], v[44:45], v[198:199] op_sel_hi:[1,0]
	v_pk_mul_f32 v[42:43], v[42:43], v[198:199] op_sel_hi:[1,0]
	v_pk_mul_f32 v[32:33], v[32:33], v[198:199] op_sel_hi:[1,0]
	v_pk_mul_f32 v[30:31], v[30:31], v[198:199] op_sel_hi:[1,0]
	v_pk_mul_f32 v[54:55], v[28:29], v[198:199] op_sel_hi:[1,0]
	v_pk_mul_f32 v[50:51], v[26:27], v[198:199] op_sel_hi:[1,0]
	v_cvt_pk_bf16_f32 v26, v46, v47
	v_cvt_pk_bf16_f32 v27, v48, v49
	v_cvt_pk_bf16_f32 v28, v42, v43
	v_cvt_pk_bf16_f32 v29, v44, v45
	global_store_dwordx4 v[52:53], v[26:29], off
	s_nop 1
	v_cvt_pk_bf16_f32 v26, v30, v31
	v_cvt_pk_bf16_f32 v27, v32, v33
	v_cvt_pk_bf16_f32 v28, v50, v51
	v_cvt_pk_bf16_f32 v29, v54, v55
	global_store_dwordx4 v[52:53], v[26:29], off offset:256
	s_or_b64 exec, exec, s[24:25]
	s_nop 0
	s_nop 0
	v_cmp_lt_i32_e32 vcc, -1, v200
	s_and_saveexec_b64 s[24:25], vcc
	s_nop 0
	v_lshlrev_b64 v[28:29], 12, v[200:201]
	v_mov_b32_e32 v145, v139
	v_lshl_add_u64 v[28:29], s[8:9], 0, v[28:29]
	v_lshl_add_u64 v[28:29], v[28:29], 0, v[144:145]
	s_nop 0
	v_pk_mul_f32 v[30:31], v[12:13], v[202:203] op_sel_hi:[1,0]
	v_pk_mul_f32 v[12:13], v[10:11], v[202:203] op_sel_hi:[1,0]
	v_pk_mul_f32 v[16:17], v[16:17], v[202:203] op_sel_hi:[1,0]
	v_pk_mul_f32 v[14:15], v[14:15], v[202:203] op_sel_hi:[1,0]
	v_pk_mul_f32 v[32:33], v[36:37], v[202:203] op_sel_hi:[1,0]
	v_cvt_pk_bf16_f32 v10, v14, v15
	v_cvt_pk_bf16_f32 v11, v16, v17
	v_cvt_pk_bf16_f32 v12, v12, v13
	v_cvt_pk_bf16_f32 v13, v30, v31
	v_pk_mul_f32 v[34:35], v[34:35], v[202:203] op_sel_hi:[1,0]
	v_pk_mul_f32 v[36:37], v[40:41], v[202:203] op_sel_hi:[1,0]
	v_pk_mul_f32 v[26:27], v[38:39], v[202:203] op_sel_hi:[1,0]
	global_store_dwordx4 v[28:29], v[10:13], off
	s_nop 1
	v_cvt_pk_bf16_f32 v10, v34, v35
	v_cvt_pk_bf16_f32 v11, v32, v33
	v_cvt_pk_bf16_f32 v12, v26, v27
	v_cvt_pk_bf16_f32 v13, v36, v37
	global_store_dwordx4 v[28:29], v[10:13], off offset:256
	s_or_b64 exec, exec, s[24:25]
	s_nop 0
	s_nop 0
	v_cmp_lt_i32_e32 vcc, -1, v204
	s_and_saveexec_b64 s[24:25], vcc
	s_nop 0
	v_lshlrev_b64 v[12:13], 12, v[204:205]
	v_mov_b32_e32 v145, v139
	v_lshl_add_u64 v[12:13], s[8:9], 0, v[12:13]
	v_lshl_add_u64 v[12:13], v[12:13], 0, v[144:145]
	s_nop 0
	v_pk_mul_f32 v[14:15], v[4:5], v[206:207] op_sel_hi:[1,0]
	v_pk_mul_f32 v[4:5], v[2:3], v[206:207] op_sel_hi:[1,0]
	v_pk_mul_f32 v[8:9], v[8:9], v[206:207] op_sel_hi:[1,0]
	v_pk_mul_f32 v[6:7], v[6:7], v[206:207] op_sel_hi:[1,0]
	v_pk_mul_f32 v[16:17], v[20:21], v[206:207] op_sel_hi:[1,0]
	v_cvt_pk_bf16_f32 v2, v6, v7
	v_cvt_pk_bf16_f32 v3, v8, v9
	v_cvt_pk_bf16_f32 v4, v4, v5
	v_cvt_pk_bf16_f32 v5, v14, v15
	v_pk_mul_f32 v[18:19], v[18:19], v[206:207] op_sel_hi:[1,0]
	v_pk_mul_f32 v[20:21], v[24:25], v[206:207] op_sel_hi:[1,0]
	v_pk_mul_f32 v[10:11], v[22:23], v[206:207] op_sel_hi:[1,0]
	global_store_dwordx4 v[12:13], v[2:5], off
	s_nop 1
	v_cvt_pk_bf16_f32 v2, v18, v19
	v_cvt_pk_bf16_f32 v3, v16, v17
	v_cvt_pk_bf16_f32 v4, v10, v11
	v_cvt_pk_bf16_f32 v5, v20, v21
	global_store_dwordx4 v[12:13], v[2:5], off offset:256
	s_or_b64 exec, exec, s[24:25]
	s_andn2_b64 vcc, exec, s[18:19]
	s_mov_b64 s[18:19], -1
	s_cbranch_vccnz .LBB0_992
	s_andn2_b64 vcc, exec, s[2:3]
	s_cbranch_vccnz .LBB0_991
	s_barrier
	s_branch .LBB0_991
